# v119 + poolconv Y stores nt (streaming; consumed two phases later)
# baseline (speedup 1.0000x reference)
; __device__ __forceinline__ unsigned pk2(float lo, float hi) { return pg8::cvt_pk_bf16(lo, hi); }
; __device__ __forceinline__ void unpack8(const v4u w, float (&f)[8]) { f[0] = bflo(w.x); f[1] = bfhi(w.x); f[2] = bflo(w.y); f[3] = bfhi(w.y); f[4] = bflo(w.z); f[5] = bfhi(w.z); f[6] = bflo(w.w); f[7] = bfhi(w.w); }
; __device__ __forceinline__ int lane_id() { int l; asm volatile("s_nop 4\n\tv_mbcnt_lo_u32_b32 %0, -1, 0\n\tv_mbcnt_hi_u32_b32 %0, -1, %0\n\ts_nop 4" : "=v"(l)); return l; }
; template <int W> __device__ __forceinline__ void pool_item(Frame& F, int row, int t, int c8) {
;     float s[8], u[8];
; #pragma unroll
;     for (int i = 0; i < 8; ++i) s[i] = 0.f;
;     v4u ld[W];
; #pragma unroll
;     for (int k = 0; k < W; ++k) { const int kk = (t - k) >= 0 ? k : t; ld[k] = *(const v4u*)(F.PROJ + (size_t)(row - kk) * INWP + O_UPOOL + c8); }
; #pragma unroll
;     for (int k = W - 1; k >= 0; --k) { unpack8(ld[k], u); const float wgt = (t - k) >= 0 ? 1.f : 0.f;
; #pragma unroll
;         for (int i = 0; i < 8; ++i) s[i] += wgt * u[i]; }
;     const int cnt = (t + 1) < W ? (t + 1) : W;
;     const float inv = 1.0f / (float)cnt;
;     v4u o; o.x = pk2(s[0] * inv - u[0], s[1] * inv - u[1]); o.y = pk2(s[2] * inv - u[2], s[3] * inv - u[3]); o.z = pk2(s[4] * inv - u[4], s[5] * inv - u[5]); o.w = pk2(s[6] * inv - u[6], s[7] * inv - u[7]);
;     *(v4u*)(F.Y + (size_t)row * 1024 + c8) = o;
; }
; __device__ __forceinline__ void poolconv_phase(Frame& F, const float* conv_w_l) {
;     int tid = F.wave * 64 + lane_id(); asm volatile("" : "+v"(tid));
;     const int gt = F.vcu * NTHR + tid, NGT = F.G * NTHR;
;     for (int idx = gt; idx < M * 128; idx += NGT) {
;         const int grp = idx / (M * 32), rem = idx - grp * (M * 32), row = rem >> 5, c8 = grp * 256 + (rem & 31) * 8, t = row & (SEQ - 1);
;         if (grp == 0) pool_item<2>(F, row, t, c8); else if (grp == 1) pool_item<4>(F, row, t, c8); else if (grp == 2) pool_item<8>(F, row, t, c8); else pool_item<16>(F, row, t, c8);
;     }
.LBB0_239:
	v_readlane_b32 s0, v255, 42
	s_add_i32 s4, s0, 2
	v_readlane_b32 s0, v251, 14
	v_readlane_b32 s1, v251, 15
	s_cmp_le_i32 s0, s4
	s_cselect_b64 s[2:3], -1, 0
	s_cmp_lt_i32 s4, s1
	s_cselect_b64 s[4:5], -1, 0
	s_mov_b32 s1, s63
	s_and_b64 s[2:3], s[2:3], s[4:5]
	v_writelane_b32 v255, s0, 45
	s_andn2_b64 vcc, exec, s[2:3]
	s_nop 0
	v_writelane_b32 v255, s1, 46
	s_cbranch_vccnz .LBB0_540
	v_mbcnt_lo_u32_b32 v0, -1, 0
	v_mbcnt_hi_u32_b32 v0, -1, v0
	v_readlane_b32 s0, v255, 12
	v_readlane_b32 s14, v251, 40
	v_readlane_b32 s15, v251, 41
	v_readlane_b32 s10, v255, 43
	s_and_b32 s1, s0, 7
	s_lshl_b32 s1, s1, 5
	s_lshr_b32 s0, s0, 3
	s_or_b32 s1, s1, s0
	s_lshl_b32 s2, s1, 9
	s_lshl_b32 s3, s35, 6
	s_add_i32 s2, s2, s3
	v_add_u32_e32 v1, s2, v0
	s_lshr_b32 s3, s1, 7
	v_and_b32_e32 v2, 0xffff, v1
	v_lshrrev_b32_e32 v2, 5, v2
	v_and_b32_e32 v3, 31, v1
	v_lshlrev_b32_e32 v4, 2, v2
	v_and_b32_e32 v5, 0x7ff, v4
	v_mul_u32_u24_e32 v6, 0x3600, v5
	v_mul_u32_u24_e32 v7, 0x3600, v4
	v_lshlrev_b32_e32 v8, 4, v3
	v_lshl_add_u32 v9, v4, 11, v8
	v_add_u32_e32 v7, v7, v8
	s_cmp_eq_u32 s3, 0
	s_cbranch_scc0 .Lpc_g1
	v_add_u32_e32 v14, 0x0, v7
	v_add_u32_e32 v15, 0x600, v7
	v_add_u32_e32 v16, 0x0, v9
	v_add_u32_e32 v17, 0x600, v9
	v_min_u32_e32 v11, 0x3600, v6
	v_sub_u32_e32 v12, v14, v11
	global_load_dwordx4 v[20:23], v12, s[96:97] nt
	global_load_dwordx4 v[24:27], v14, s[96:97] nt
	v_add_u32_e32 v12, 0x3600, v14
	global_load_dwordx4 v[28:31], v12, s[96:97] nt
	v_add_u32_e32 v12, 0x6c00, v14
	global_load_dwordx4 v[32:35], v12, s[96:97] nt
	v_add_u32_e32 v12, 0xa200, v14
	global_load_dwordx4 v[36:39], v12, s[96:97] nt
	v_min_u32_e32 v11, 0x32a00, v6
	v_sub_u32_e32 v12, v15, v11
	global_load_dwordx4 v[48:51], v12, s[96:97] nt
	v_min_u32_e32 v11, 0x2f400, v6
	v_sub_u32_e32 v12, v15, v11
	global_load_dwordx4 v[52:55], v12, s[96:97] nt
	v_min_u32_e32 v11, 0x2be00, v6
	v_sub_u32_e32 v12, v15, v11
	global_load_dwordx4 v[56:59], v12, s[96:97] nt
	v_min_u32_e32 v11, 0x28800, v6
	v_sub_u32_e32 v12, v15, v11
	global_load_dwordx4 v[60:63], v12, s[96:97] nt
	v_min_u32_e32 v11, 0x25200, v6
	v_sub_u32_e32 v12, v15, v11
	global_load_dwordx4 v[64:67], v12, s[96:97] nt
	v_min_u32_e32 v11, 0x21c00, v6
	v_sub_u32_e32 v12, v15, v11
	global_load_dwordx4 v[68:71], v12, s[96:97] nt
	v_min_u32_e32 v11, 0x1e600, v6
	v_sub_u32_e32 v12, v15, v11
	global_load_dwordx4 v[72:75], v12, s[96:97] nt
	v_min_u32_e32 v11, 0x1b000, v6
	v_sub_u32_e32 v12, v15, v11
	global_load_dwordx4 v[76:79], v12, s[96:97] nt
	v_min_u32_e32 v11, 0x17a00, v6
	v_sub_u32_e32 v12, v15, v11
	global_load_dwordx4 v[80:83], v12, s[96:97] nt
	v_min_u32_e32 v11, 0x14400, v6
	v_sub_u32_e32 v12, v15, v11
	global_load_dwordx4 v[84:87], v12, s[96:97] nt
	v_min_u32_e32 v11, 0x10e00, v6
	v_sub_u32_e32 v12, v15, v11
	global_load_dwordx4 v[88:91], v12, s[96:97] nt
	v_min_u32_e32 v11, 0xd800, v6
	v_sub_u32_e32 v12, v15, v11
	global_load_dwordx4 v[92:95], v12, s[96:97] nt
	v_min_u32_e32 v11, 0xa200, v6
	v_sub_u32_e32 v12, v15, v11
	global_load_dwordx4 v[96:99], v12, s[96:97] nt
	v_min_u32_e32 v11, 0x6c00, v6
	v_sub_u32_e32 v12, v15, v11
	global_load_dwordx4 v[100:103], v12, s[96:97] nt
	v_min_u32_e32 v11, 0x3600, v6
	v_sub_u32_e32 v12, v15, v11
	global_load_dwordx4 v[104:107], v12, s[96:97] nt
	global_load_dwordx4 v[108:111], v15, s[96:97] nt
	v_add_u32_e32 v12, 0x3600, v15
	global_load_dwordx4 v[112:115], v12, s[96:97] nt
	v_add_u32_e32 v12, 0x6c00, v15
	global_load_dwordx4 v[116:119], v12, s[96:97] nt
	v_add_u32_e32 v12, 0xa200, v15
	global_load_dwordx4 v[120:123], v12, s[96:97] nt
	s_waitcnt vmcnt(19)
	v_cmp_le_u32_e32 vcc, 1, v5
	s_nop 1
	v_cndmask_b32_e32 v20, 0, v20, vcc
	v_cndmask_b32_e32 v21, 0, v21, vcc
	v_cndmask_b32_e32 v22, 0, v22, vcc
	v_cndmask_b32_e32 v23, 0, v23, vcc
	v_add_u32_e32 v226, 1, v5
	v_min_u32_e32 v226, 2, v226
	v_cvt_f32_u32_e32 v226, v226
	v_rcp_f32_e32 v226, v226
	v_add_u32_e32 v227, 2, v5
	v_min_u32_e32 v227, 2, v227
	v_cvt_f32_u32_e32 v227, v227
	v_rcp_f32_e32 v227, v227
	v_add_u32_e32 v228, 3, v5
	v_min_u32_e32 v228, 2, v228
	v_cvt_f32_u32_e32 v228, v228
	v_rcp_f32_e32 v228, v228
	v_add_u32_e32 v229, 4, v5
	v_min_u32_e32 v229, 2, v229
	v_cvt_f32_u32_e32 v229, v229
	v_rcp_f32_e32 v229, v229
	v_lshlrev_b32_e32 v124, 16, v20
	v_and_b32_e32 v125, 0xffff0000, v20
	v_lshlrev_b32_e32 v126, 16, v24
	v_and_b32_e32 v127, 0xffff0000, v24
	v_lshlrev_b32_e32 v128, 16, v28
	v_and_b32_e32 v129, 0xffff0000, v28
	v_lshlrev_b32_e32 v130, 16, v32
	v_and_b32_e32 v131, 0xffff0000, v32
	v_lshlrev_b32_e32 v132, 16, v36
	v_and_b32_e32 v133, 0xffff0000, v36
	v_add_f32_e32 v194, v124, v126
	v_fma_f32 v194, v194, v226, -v126
	v_add_f32_e32 v195, v125, v127
	v_fma_f32 v195, v195, v226, -v127
	v_add_f32_e32 v202, v126, v128
	v_fma_f32 v202, v202, v227, -v128
	v_add_f32_e32 v203, v127, v129
	v_fma_f32 v203, v203, v227, -v129
	v_add_f32_e32 v210, v128, v130
	v_fma_f32 v210, v210, v228, -v130
	v_add_f32_e32 v211, v129, v131
	v_fma_f32 v211, v211, v228, -v131
	v_add_f32_e32 v218, v130, v132
	v_fma_f32 v218, v218, v229, -v132
	v_add_f32_e32 v219, v131, v133
	v_fma_f32 v219, v219, v229, -v133
	v_lshlrev_b32_e32 v124, 16, v21
	v_and_b32_e32 v125, 0xffff0000, v21
	v_lshlrev_b32_e32 v126, 16, v25
	v_and_b32_e32 v127, 0xffff0000, v25
	v_lshlrev_b32_e32 v128, 16, v29
	v_and_b32_e32 v129, 0xffff0000, v29
	v_lshlrev_b32_e32 v130, 16, v33
	v_and_b32_e32 v131, 0xffff0000, v33
	v_lshlrev_b32_e32 v132, 16, v37
	v_and_b32_e32 v133, 0xffff0000, v37
	v_add_f32_e32 v196, v124, v126
	v_fma_f32 v196, v196, v226, -v126
	v_add_f32_e32 v197, v125, v127
	v_fma_f32 v197, v197, v226, -v127
	v_add_f32_e32 v204, v126, v128
	v_fma_f32 v204, v204, v227, -v128
; __device__ __forceinline__ unsigned pk2(float lo, float hi) { return pg8::cvt_pk_bf16(lo, hi); }
; __device__ __forceinline__ void unpack8(const v4u w, float (&f)[8]) { f[0] = bflo(w.x); f[1] = bfhi(w.x); f[2] = bflo(w.y); f[3] = bfhi(w.y); f[4] = bflo(w.z); f[5] = bfhi(w.z); f[6] = bflo(w.w); f[7] = bfhi(w.w); }
; template <int W> __device__ __forceinline__ void pool_item(Frame& F, int row, int t, int c8) {
;     float s[8], u[8];
; #pragma unroll
;     for (int i = 0; i < 8; ++i) s[i] = 0.f;
;     v4u ld[W];
; #pragma unroll
;     for (int k = 0; k < W; ++k) { const int kk = (t - k) >= 0 ? k : t; ld[k] = *(const v4u*)(F.PROJ + (size_t)(row - kk) * INWP + O_UPOOL + c8); }
; #pragma unroll
;     for (int k = W - 1; k >= 0; --k) { unpack8(ld[k], u); const float wgt = (t - k) >= 0 ? 1.f : 0.f;
; #pragma unroll
;         for (int i = 0; i < 8; ++i) s[i] += wgt * u[i]; }
;     const int cnt = (t + 1) < W ? (t + 1) : W;
;     const float inv = 1.0f / (float)cnt;
;     v4u o; o.x = pk2(s[0] * inv - u[0], s[1] * inv - u[1]); o.y = pk2(s[2] * inv - u[2], s[3] * inv - u[3]); o.z = pk2(s[4] * inv - u[4], s[5] * inv - u[5]); o.w = pk2(s[6] * inv - u[6], s[7] * inv - u[7]);
;     *(v4u*)(F.Y + (size_t)row * 1024 + c8) = o;
; }
	v_add_f32_e32 v205, v127, v129
	v_fma_f32 v205, v205, v227, -v129
	v_add_f32_e32 v212, v128, v130
	v_fma_f32 v212, v212, v228, -v130
	v_add_f32_e32 v213, v129, v131
	v_fma_f32 v213, v213, v228, -v131
	v_add_f32_e32 v220, v130, v132
	v_fma_f32 v220, v220, v229, -v132
	v_add_f32_e32 v221, v131, v133
	v_fma_f32 v221, v221, v229, -v133
	v_lshlrev_b32_e32 v124, 16, v22
	v_and_b32_e32 v125, 0xffff0000, v22
	v_lshlrev_b32_e32 v126, 16, v26
	v_and_b32_e32 v127, 0xffff0000, v26
	v_lshlrev_b32_e32 v128, 16, v30
	v_and_b32_e32 v129, 0xffff0000, v30
	v_lshlrev_b32_e32 v130, 16, v34
	v_and_b32_e32 v131, 0xffff0000, v34
	v_lshlrev_b32_e32 v132, 16, v38
	v_and_b32_e32 v133, 0xffff0000, v38
	v_add_f32_e32 v198, v124, v126
	v_fma_f32 v198, v198, v226, -v126
	v_add_f32_e32 v199, v125, v127
	v_fma_f32 v199, v199, v226, -v127
	v_add_f32_e32 v206, v126, v128
	v_fma_f32 v206, v206, v227, -v128
	v_add_f32_e32 v207, v127, v129
	v_fma_f32 v207, v207, v227, -v129
	v_add_f32_e32 v214, v128, v130
	v_fma_f32 v214, v214, v228, -v130
	v_add_f32_e32 v215, v129, v131
	v_fma_f32 v215, v215, v228, -v131
	v_add_f32_e32 v222, v130, v132
	v_fma_f32 v222, v222, v229, -v132
	v_add_f32_e32 v223, v131, v133
	v_fma_f32 v223, v223, v229, -v133
	v_lshlrev_b32_e32 v124, 16, v23
	v_and_b32_e32 v125, 0xffff0000, v23
	v_lshlrev_b32_e32 v126, 16, v27
	v_and_b32_e32 v127, 0xffff0000, v27
	v_lshlrev_b32_e32 v128, 16, v31
	v_and_b32_e32 v129, 0xffff0000, v31
	v_lshlrev_b32_e32 v130, 16, v35
	v_and_b32_e32 v131, 0xffff0000, v35
	v_lshlrev_b32_e32 v132, 16, v39
	v_and_b32_e32 v133, 0xffff0000, v39
	v_add_f32_e32 v200, v124, v126
	v_fma_f32 v200, v200, v226, -v126
	v_add_f32_e32 v201, v125, v127
	v_fma_f32 v201, v201, v226, -v127
	v_add_f32_e32 v208, v126, v128
	v_fma_f32 v208, v208, v227, -v128
	v_add_f32_e32 v209, v127, v129
	v_fma_f32 v209, v209, v227, -v129
	v_add_f32_e32 v216, v128, v130
	v_fma_f32 v216, v216, v228, -v130
	v_add_f32_e32 v217, v129, v131
	v_fma_f32 v217, v217, v228, -v131
	v_add_f32_e32 v224, v130, v132
	v_fma_f32 v224, v224, v229, -v132
	v_add_f32_e32 v225, v131, v133
	v_fma_f32 v225, v225, v229, -v133
	v_cvt_pk_bf16_f32 v194, v194, v195
	v_cvt_pk_bf16_f32 v195, v196, v197
	v_cvt_pk_bf16_f32 v196, v198, v199
	v_cvt_pk_bf16_f32 v197, v200, v201
	global_store_dwordx4 v16, v[194:197], s[14:15] nt
	v_cvt_pk_bf16_f32 v202, v202, v203
	v_cvt_pk_bf16_f32 v203, v204, v205
	v_cvt_pk_bf16_f32 v204, v206, v207
	v_cvt_pk_bf16_f32 v205, v208, v209
	v_add_u32_e32 v13, 0x800, v16
	global_store_dwordx4 v13, v[202:205], s[14:15] nt
	v_cvt_pk_bf16_f32 v210, v210, v211
	v_cvt_pk_bf16_f32 v211, v212, v213
	v_cvt_pk_bf16_f32 v212, v214, v215
	v_cvt_pk_bf16_f32 v213, v216, v217
	v_add_u32_e32 v13, 0x1000, v16
	global_store_dwordx4 v13, v[210:213], s[14:15] nt
	v_cvt_pk_bf16_f32 v218, v218, v219
	v_cvt_pk_bf16_f32 v219, v220, v221
	v_cvt_pk_bf16_f32 v220, v222, v223
	v_cvt_pk_bf16_f32 v221, v224, v225
	v_add_u32_e32 v13, 0x1800, v16
	global_store_dwordx4 v13, v[218:221], s[14:15] nt
	s_waitcnt vmcnt(4)
	v_cmp_le_u32_e32 vcc, 15, v5
	s_nop 1
	v_cndmask_b32_e32 v48, 0, v48, vcc
	v_cndmask_b32_e32 v49, 0, v49, vcc
	v_cndmask_b32_e32 v50, 0, v50, vcc
	v_cndmask_b32_e32 v51, 0, v51, vcc
	v_cmp_le_u32_e32 vcc, 14, v5
	s_nop 1
	v_cndmask_b32_e32 v52, 0, v52, vcc
	v_cndmask_b32_e32 v53, 0, v53, vcc
	v_cndmask_b32_e32 v54, 0, v54, vcc
	v_cndmask_b32_e32 v55, 0, v55, vcc
	v_cmp_le_u32_e32 vcc, 13, v5
	s_nop 1
	v_cndmask_b32_e32 v56, 0, v56, vcc
	v_cndmask_b32_e32 v57, 0, v57, vcc
	v_cndmask_b32_e32 v58, 0, v58, vcc
	v_cndmask_b32_e32 v59, 0, v59, vcc
	v_cmp_le_u32_e32 vcc, 12, v5
	s_nop 1
	v_cndmask_b32_e32 v60, 0, v60, vcc
	v_cndmask_b32_e32 v61, 0, v61, vcc
	v_cndmask_b32_e32 v62, 0, v62, vcc
	v_cndmask_b32_e32 v63, 0, v63, vcc
	v_cmp_le_u32_e32 vcc, 11, v5
	s_nop 1
	v_cndmask_b32_e32 v64, 0, v64, vcc
	v_cndmask_b32_e32 v65, 0, v65, vcc
	v_cndmask_b32_e32 v66, 0, v66, vcc
	v_cndmask_b32_e32 v67, 0, v67, vcc
	v_cmp_le_u32_e32 vcc, 10, v5
	s_nop 1
	v_cndmask_b32_e32 v68, 0, v68, vcc
	v_cndmask_b32_e32 v69, 0, v69, vcc
	v_cndmask_b32_e32 v70, 0, v70, vcc
	v_cndmask_b32_e32 v71, 0, v71, vcc
	v_cmp_le_u32_e32 vcc, 9, v5
	s_nop 1
	v_cndmask_b32_e32 v72, 0, v72, vcc
	v_cndmask_b32_e32 v73, 0, v73, vcc
	v_cndmask_b32_e32 v74, 0, v74, vcc
	v_cndmask_b32_e32 v75, 0, v75, vcc
	v_cmp_le_u32_e32 vcc, 8, v5
	s_nop 1
	v_cndmask_b32_e32 v76, 0, v76, vcc
	v_cndmask_b32_e32 v77, 0, v77, vcc
	v_cndmask_b32_e32 v78, 0, v78, vcc
	v_cndmask_b32_e32 v79, 0, v79, vcc
	v_cmp_le_u32_e32 vcc, 7, v5
	s_nop 1
	v_cndmask_b32_e32 v80, 0, v80, vcc
	v_cndmask_b32_e32 v81, 0, v81, vcc
	v_cndmask_b32_e32 v82, 0, v82, vcc
	v_cndmask_b32_e32 v83, 0, v83, vcc
	v_cmp_le_u32_e32 vcc, 6, v5
	s_nop 1
	v_cndmask_b32_e32 v84, 0, v84, vcc
	v_cndmask_b32_e32 v85, 0, v85, vcc
	v_cndmask_b32_e32 v86, 0, v86, vcc
	v_cndmask_b32_e32 v87, 0, v87, vcc
	v_cmp_le_u32_e32 vcc, 5, v5
	s_nop 1
	v_cndmask_b32_e32 v88, 0, v88, vcc
	v_cndmask_b32_e32 v89, 0, v89, vcc
	v_cndmask_b32_e32 v90, 0, v90, vcc
	v_cndmask_b32_e32 v91, 0, v91, vcc
	v_cmp_le_u32_e32 vcc, 4, v5
	s_nop 1
	v_cndmask_b32_e32 v92, 0, v92, vcc
	v_cndmask_b32_e32 v93, 0, v93, vcc
	v_cndmask_b32_e32 v94, 0, v94, vcc
	v_cndmask_b32_e32 v95, 0, v95, vcc
	v_cmp_le_u32_e32 vcc, 3, v5
	s_nop 1
	v_cndmask_b32_e32 v96, 0, v96, vcc
	v_cndmask_b32_e32 v97, 0, v97, vcc
	v_cndmask_b32_e32 v98, 0, v98, vcc
	v_cndmask_b32_e32 v99, 0, v99, vcc
	v_cmp_le_u32_e32 vcc, 2, v5
	s_nop 1
	v_cndmask_b32_e32 v100, 0, v100, vcc
	v_cndmask_b32_e32 v101, 0, v101, vcc
	v_cndmask_b32_e32 v102, 0, v102, vcc
	v_cndmask_b32_e32 v103, 0, v103, vcc
	v_cmp_le_u32_e32 vcc, 1, v5
	s_nop 1
	v_cndmask_b32_e32 v104, 0, v104, vcc
; __device__ __forceinline__ unsigned pk2(float lo, float hi) { return pg8::cvt_pk_bf16(lo, hi); }
; __device__ __forceinline__ void unpack8(const v4u w, float (&f)[8]) { f[0] = bflo(w.x); f[1] = bfhi(w.x); f[2] = bflo(w.y); f[3] = bfhi(w.y); f[4] = bflo(w.z); f[5] = bfhi(w.z); f[6] = bflo(w.w); f[7] = bfhi(w.w); }
; template <int W> __device__ __forceinline__ void pool_item(Frame& F, int row, int t, int c8) {
;     float s[8], u[8];
; #pragma unroll
;     for (int i = 0; i < 8; ++i) s[i] = 0.f;
;     v4u ld[W];
; #pragma unroll
;     for (int k = 0; k < W; ++k) { const int kk = (t - k) >= 0 ? k : t; ld[k] = *(const v4u*)(F.PROJ + (size_t)(row - kk) * INWP + O_UPOOL + c8); }
; #pragma unroll
;     for (int k = W - 1; k >= 0; --k) { unpack8(ld[k], u); const float wgt = (t - k) >= 0 ? 1.f : 0.f;
; #pragma unroll
;         for (int i = 0; i < 8; ++i) s[i] += wgt * u[i]; }
;     const int cnt = (t + 1) < W ? (t + 1) : W;
;     const float inv = 1.0f / (float)cnt;
;     v4u o; o.x = pk2(s[0] * inv - u[0], s[1] * inv - u[1]); o.y = pk2(s[2] * inv - u[2], s[3] * inv - u[3]); o.z = pk2(s[4] * inv - u[4], s[5] * inv - u[5]); o.w = pk2(s[6] * inv - u[6], s[7] * inv - u[7]);
;     *(v4u*)(F.Y + (size_t)row * 1024 + c8) = o;
; }
	v_cndmask_b32_e32 v105, 0, v105, vcc
	v_cndmask_b32_e32 v106, 0, v106, vcc
	v_cndmask_b32_e32 v107, 0, v107, vcc
	v_add_u32_e32 v226, 1, v5
	v_min_u32_e32 v226, 16, v226
	v_cvt_f32_u32_e32 v226, v226
	v_rcp_f32_e32 v226, v226
	v_add_u32_e32 v227, 2, v5
	v_min_u32_e32 v227, 16, v227
	v_cvt_f32_u32_e32 v227, v227
	v_rcp_f32_e32 v227, v227
	v_add_u32_e32 v228, 3, v5
	v_min_u32_e32 v228, 16, v228
	v_cvt_f32_u32_e32 v228, v228
	v_rcp_f32_e32 v228, v228
	v_add_u32_e32 v229, 4, v5
	v_min_u32_e32 v229, 16, v229
	v_cvt_f32_u32_e32 v229, v229
	v_rcp_f32_e32 v229, v229
	v_lshlrev_b32_e32 v124, 16, v48
	v_and_b32_e32 v125, 0xffff0000, v48
	v_lshlrev_b32_e32 v126, 16, v52
	v_and_b32_e32 v127, 0xffff0000, v52
	v_lshlrev_b32_e32 v128, 16, v56
	v_and_b32_e32 v129, 0xffff0000, v56
	v_lshlrev_b32_e32 v130, 16, v60
	v_and_b32_e32 v131, 0xffff0000, v60
	v_lshlrev_b32_e32 v132, 16, v64
	v_and_b32_e32 v133, 0xffff0000, v64
	v_lshlrev_b32_e32 v134, 16, v68
	v_and_b32_e32 v135, 0xffff0000, v68
	v_lshlrev_b32_e32 v136, 16, v72
	v_and_b32_e32 v137, 0xffff0000, v72
	v_lshlrev_b32_e32 v138, 16, v76
	v_and_b32_e32 v139, 0xffff0000, v76
	v_lshlrev_b32_e32 v140, 16, v80
	v_and_b32_e32 v141, 0xffff0000, v80
	v_lshlrev_b32_e32 v142, 16, v84
	v_and_b32_e32 v143, 0xffff0000, v84
	v_lshlrev_b32_e32 v144, 16, v88
	v_and_b32_e32 v145, 0xffff0000, v88
	v_lshlrev_b32_e32 v146, 16, v92
	v_and_b32_e32 v147, 0xffff0000, v92
	v_lshlrev_b32_e32 v148, 16, v96
	v_and_b32_e32 v149, 0xffff0000, v96
	v_lshlrev_b32_e32 v150, 16, v100
	v_and_b32_e32 v151, 0xffff0000, v100
	v_lshlrev_b32_e32 v152, 16, v104
	v_and_b32_e32 v153, 0xffff0000, v104
	v_lshlrev_b32_e32 v154, 16, v108
	v_and_b32_e32 v155, 0xffff0000, v108
	v_lshlrev_b32_e32 v156, 16, v112
	v_and_b32_e32 v157, 0xffff0000, v112
	v_lshlrev_b32_e32 v158, 16, v116
	v_and_b32_e32 v159, 0xffff0000, v116
	v_lshlrev_b32_e32 v160, 16, v120
	v_and_b32_e32 v161, 0xffff0000, v120
	v_add_f32_e32 v194, v124, v126
	v_add_f32_e32 v194, v194, v128
	v_add_f32_e32 v194, v194, v130
	v_add_f32_e32 v194, v194, v132
	v_add_f32_e32 v194, v194, v134
	v_add_f32_e32 v194, v194, v136
	v_add_f32_e32 v194, v194, v138
	v_add_f32_e32 v194, v194, v140
	v_add_f32_e32 v194, v194, v142
	v_add_f32_e32 v194, v194, v144
	v_add_f32_e32 v194, v194, v146
	v_add_f32_e32 v194, v194, v148
	v_add_f32_e32 v194, v194, v150
	v_add_f32_e32 v194, v194, v152
	v_add_f32_e32 v194, v194, v154
	v_fma_f32 v194, v194, v226, -v154
	v_add_f32_e32 v195, v125, v127
	v_add_f32_e32 v195, v195, v129
	v_add_f32_e32 v195, v195, v131
	v_add_f32_e32 v195, v195, v133
	v_add_f32_e32 v195, v195, v135
	v_add_f32_e32 v195, v195, v137
	v_add_f32_e32 v195, v195, v139
	v_add_f32_e32 v195, v195, v141
	v_add_f32_e32 v195, v195, v143
	v_add_f32_e32 v195, v195, v145
	v_add_f32_e32 v195, v195, v147
	v_add_f32_e32 v195, v195, v149
	v_add_f32_e32 v195, v195, v151
	v_add_f32_e32 v195, v195, v153
	v_add_f32_e32 v195, v195, v155
	v_fma_f32 v195, v195, v226, -v155
	v_add_f32_e32 v202, v126, v128
	v_add_f32_e32 v202, v202, v130
	v_add_f32_e32 v202, v202, v132
	v_add_f32_e32 v202, v202, v134
	v_add_f32_e32 v202, v202, v136
	v_add_f32_e32 v202, v202, v138
	v_add_f32_e32 v202, v202, v140
	v_add_f32_e32 v202, v202, v142
	v_add_f32_e32 v202, v202, v144
	v_add_f32_e32 v202, v202, v146
	v_add_f32_e32 v202, v202, v148
	v_add_f32_e32 v202, v202, v150
	v_add_f32_e32 v202, v202, v152
	v_add_f32_e32 v202, v202, v154
	v_add_f32_e32 v202, v202, v156
	v_fma_f32 v202, v202, v227, -v156
	v_add_f32_e32 v203, v127, v129
	v_add_f32_e32 v203, v203, v131
	v_add_f32_e32 v203, v203, v133
	v_add_f32_e32 v203, v203, v135
	v_add_f32_e32 v203, v203, v137
	v_add_f32_e32 v203, v203, v139
	v_add_f32_e32 v203, v203, v141
	v_add_f32_e32 v203, v203, v143
	v_add_f32_e32 v203, v203, v145
	v_add_f32_e32 v203, v203, v147
	v_add_f32_e32 v203, v203, v149
	v_add_f32_e32 v203, v203, v151
	v_add_f32_e32 v203, v203, v153
	v_add_f32_e32 v203, v203, v155
	v_add_f32_e32 v203, v203, v157
	v_fma_f32 v203, v203, v227, -v157
	v_add_f32_e32 v210, v128, v130
	v_add_f32_e32 v210, v210, v132
	v_add_f32_e32 v210, v210, v134
	v_add_f32_e32 v210, v210, v136
	v_add_f32_e32 v210, v210, v138
	v_add_f32_e32 v210, v210, v140
	v_add_f32_e32 v210, v210, v142
	v_add_f32_e32 v210, v210, v144
	v_add_f32_e32 v210, v210, v146
	v_add_f32_e32 v210, v210, v148
	v_add_f32_e32 v210, v210, v150
	v_add_f32_e32 v210, v210, v152
	v_add_f32_e32 v210, v210, v154
	v_add_f32_e32 v210, v210, v156
	v_add_f32_e32 v210, v210, v158
	v_fma_f32 v210, v210, v228, -v158
	v_add_f32_e32 v211, v129, v131
	v_add_f32_e32 v211, v211, v133
	v_add_f32_e32 v211, v211, v135
	v_add_f32_e32 v211, v211, v137
	v_add_f32_e32 v211, v211, v139
	v_add_f32_e32 v211, v211, v141
	v_add_f32_e32 v211, v211, v143
	v_add_f32_e32 v211, v211, v145
	v_add_f32_e32 v211, v211, v147
	v_add_f32_e32 v211, v211, v149
	v_add_f32_e32 v211, v211, v151
	v_add_f32_e32 v211, v211, v153
	v_add_f32_e32 v211, v211, v155
	v_add_f32_e32 v211, v211, v157
	v_add_f32_e32 v211, v211, v159
	v_fma_f32 v211, v211, v228, -v159
	v_add_f32_e32 v218, v130, v132
	v_add_f32_e32 v218, v218, v134
	v_add_f32_e32 v218, v218, v136
	v_add_f32_e32 v218, v218, v138
	v_add_f32_e32 v218, v218, v140
	v_add_f32_e32 v218, v218, v142
	v_add_f32_e32 v218, v218, v144
	v_add_f32_e32 v218, v218, v146
	v_add_f32_e32 v218, v218, v148
	v_add_f32_e32 v218, v218, v150
	v_add_f32_e32 v218, v218, v152
	v_add_f32_e32 v218, v218, v154
	v_add_f32_e32 v218, v218, v156
	v_add_f32_e32 v218, v218, v158
	v_add_f32_e32 v218, v218, v160
	v_fma_f32 v218, v218, v229, -v160
	v_add_f32_e32 v219, v131, v133
	v_add_f32_e32 v219, v219, v135
	v_add_f32_e32 v219, v219, v137
	v_add_f32_e32 v219, v219, v139
; __device__ __forceinline__ unsigned pk2(float lo, float hi) { return pg8::cvt_pk_bf16(lo, hi); }
; __device__ __forceinline__ void unpack8(const v4u w, float (&f)[8]) { f[0] = bflo(w.x); f[1] = bfhi(w.x); f[2] = bflo(w.y); f[3] = bfhi(w.y); f[4] = bflo(w.z); f[5] = bfhi(w.z); f[6] = bflo(w.w); f[7] = bfhi(w.w); }
; template <int W> __device__ __forceinline__ void pool_item(Frame& F, int row, int t, int c8) {
;     float s[8], u[8];
; #pragma unroll
;     for (int i = 0; i < 8; ++i) s[i] = 0.f;
;     v4u ld[W];
; #pragma unroll
;     for (int k = 0; k < W; ++k) { const int kk = (t - k) >= 0 ? k : t; ld[k] = *(const v4u*)(F.PROJ + (size_t)(row - kk) * INWP + O_UPOOL + c8); }
; #pragma unroll
;     for (int k = W - 1; k >= 0; --k) { unpack8(ld[k], u); const float wgt = (t - k) >= 0 ? 1.f : 0.f;
; #pragma unroll
;         for (int i = 0; i < 8; ++i) s[i] += wgt * u[i]; }
;     const int cnt = (t + 1) < W ? (t + 1) : W;
;     const float inv = 1.0f / (float)cnt;
;     v4u o; o.x = pk2(s[0] * inv - u[0], s[1] * inv - u[1]); o.y = pk2(s[2] * inv - u[2], s[3] * inv - u[3]); o.z = pk2(s[4] * inv - u[4], s[5] * inv - u[5]); o.w = pk2(s[6] * inv - u[6], s[7] * inv - u[7]);
;     *(v4u*)(F.Y + (size_t)row * 1024 + c8) = o;
; }
	v_add_f32_e32 v219, v219, v141
	v_add_f32_e32 v219, v219, v143
	v_add_f32_e32 v219, v219, v145
	v_add_f32_e32 v219, v219, v147
	v_add_f32_e32 v219, v219, v149
	v_add_f32_e32 v219, v219, v151
	v_add_f32_e32 v219, v219, v153
	v_add_f32_e32 v219, v219, v155
	v_add_f32_e32 v219, v219, v157
	v_add_f32_e32 v219, v219, v159
	v_add_f32_e32 v219, v219, v161
	v_fma_f32 v219, v219, v229, -v161
	v_lshlrev_b32_e32 v124, 16, v49
	v_and_b32_e32 v125, 0xffff0000, v49
	v_lshlrev_b32_e32 v126, 16, v53
	v_and_b32_e32 v127, 0xffff0000, v53
	v_lshlrev_b32_e32 v128, 16, v57
	v_and_b32_e32 v129, 0xffff0000, v57
	v_lshlrev_b32_e32 v130, 16, v61
	v_and_b32_e32 v131, 0xffff0000, v61
	v_lshlrev_b32_e32 v132, 16, v65
	v_and_b32_e32 v133, 0xffff0000, v65
	v_lshlrev_b32_e32 v134, 16, v69
	v_and_b32_e32 v135, 0xffff0000, v69
	v_lshlrev_b32_e32 v136, 16, v73
	v_and_b32_e32 v137, 0xffff0000, v73
	v_lshlrev_b32_e32 v138, 16, v77
	v_and_b32_e32 v139, 0xffff0000, v77
	v_lshlrev_b32_e32 v140, 16, v81
	v_and_b32_e32 v141, 0xffff0000, v81
	v_lshlrev_b32_e32 v142, 16, v85
	v_and_b32_e32 v143, 0xffff0000, v85
	v_lshlrev_b32_e32 v144, 16, v89
	v_and_b32_e32 v145, 0xffff0000, v89
	v_lshlrev_b32_e32 v146, 16, v93
	v_and_b32_e32 v147, 0xffff0000, v93
	v_lshlrev_b32_e32 v148, 16, v97
	v_and_b32_e32 v149, 0xffff0000, v97
	v_lshlrev_b32_e32 v150, 16, v101
	v_and_b32_e32 v151, 0xffff0000, v101
	v_lshlrev_b32_e32 v152, 16, v105
	v_and_b32_e32 v153, 0xffff0000, v105
	v_lshlrev_b32_e32 v154, 16, v109
	v_and_b32_e32 v155, 0xffff0000, v109
	v_lshlrev_b32_e32 v156, 16, v113
	v_and_b32_e32 v157, 0xffff0000, v113
	v_lshlrev_b32_e32 v158, 16, v117
	v_and_b32_e32 v159, 0xffff0000, v117
	v_lshlrev_b32_e32 v160, 16, v121
	v_and_b32_e32 v161, 0xffff0000, v121
	v_add_f32_e32 v196, v124, v126
	v_add_f32_e32 v196, v196, v128
	v_add_f32_e32 v196, v196, v130
	v_add_f32_e32 v196, v196, v132
	v_add_f32_e32 v196, v196, v134
	v_add_f32_e32 v196, v196, v136
	v_add_f32_e32 v196, v196, v138
	v_add_f32_e32 v196, v196, v140
	v_add_f32_e32 v196, v196, v142
	v_add_f32_e32 v196, v196, v144
	v_add_f32_e32 v196, v196, v146
	v_add_f32_e32 v196, v196, v148
	v_add_f32_e32 v196, v196, v150
	v_add_f32_e32 v196, v196, v152
	v_add_f32_e32 v196, v196, v154
	v_fma_f32 v196, v196, v226, -v154
	v_add_f32_e32 v197, v125, v127
	v_add_f32_e32 v197, v197, v129
	v_add_f32_e32 v197, v197, v131
	v_add_f32_e32 v197, v197, v133
	v_add_f32_e32 v197, v197, v135
	v_add_f32_e32 v197, v197, v137
	v_add_f32_e32 v197, v197, v139
	v_add_f32_e32 v197, v197, v141
	v_add_f32_e32 v197, v197, v143
	v_add_f32_e32 v197, v197, v145
	v_add_f32_e32 v197, v197, v147
	v_add_f32_e32 v197, v197, v149
	v_add_f32_e32 v197, v197, v151
	v_add_f32_e32 v197, v197, v153
	v_add_f32_e32 v197, v197, v155
	v_fma_f32 v197, v197, v226, -v155
	v_add_f32_e32 v204, v126, v128
	v_add_f32_e32 v204, v204, v130
	v_add_f32_e32 v204, v204, v132
	v_add_f32_e32 v204, v204, v134
	v_add_f32_e32 v204, v204, v136
	v_add_f32_e32 v204, v204, v138
	v_add_f32_e32 v204, v204, v140
	v_add_f32_e32 v204, v204, v142
	v_add_f32_e32 v204, v204, v144
	v_add_f32_e32 v204, v204, v146
	v_add_f32_e32 v204, v204, v148
	v_add_f32_e32 v204, v204, v150
	v_add_f32_e32 v204, v204, v152
	v_add_f32_e32 v204, v204, v154
	v_add_f32_e32 v204, v204, v156
	v_fma_f32 v204, v204, v227, -v156
	v_add_f32_e32 v205, v127, v129
	v_add_f32_e32 v205, v205, v131
	v_add_f32_e32 v205, v205, v133
	v_add_f32_e32 v205, v205, v135
	v_add_f32_e32 v205, v205, v137
	v_add_f32_e32 v205, v205, v139
	v_add_f32_e32 v205, v205, v141
	v_add_f32_e32 v205, v205, v143
	v_add_f32_e32 v205, v205, v145
	v_add_f32_e32 v205, v205, v147
	v_add_f32_e32 v205, v205, v149
	v_add_f32_e32 v205, v205, v151
	v_add_f32_e32 v205, v205, v153
	v_add_f32_e32 v205, v205, v155
	v_add_f32_e32 v205, v205, v157
	v_fma_f32 v205, v205, v227, -v157
	v_add_f32_e32 v212, v128, v130
	v_add_f32_e32 v212, v212, v132
	v_add_f32_e32 v212, v212, v134
	v_add_f32_e32 v212, v212, v136
	v_add_f32_e32 v212, v212, v138
	v_add_f32_e32 v212, v212, v140
	v_add_f32_e32 v212, v212, v142
	v_add_f32_e32 v212, v212, v144
	v_add_f32_e32 v212, v212, v146
	v_add_f32_e32 v212, v212, v148
	v_add_f32_e32 v212, v212, v150
	v_add_f32_e32 v212, v212, v152
	v_add_f32_e32 v212, v212, v154
	v_add_f32_e32 v212, v212, v156
	v_add_f32_e32 v212, v212, v158
	v_fma_f32 v212, v212, v228, -v158
	v_add_f32_e32 v213, v129, v131
	v_add_f32_e32 v213, v213, v133
	v_add_f32_e32 v213, v213, v135
	v_add_f32_e32 v213, v213, v137
	v_add_f32_e32 v213, v213, v139
	v_add_f32_e32 v213, v213, v141
	v_add_f32_e32 v213, v213, v143
	v_add_f32_e32 v213, v213, v145
	v_add_f32_e32 v213, v213, v147
	v_add_f32_e32 v213, v213, v149
	v_add_f32_e32 v213, v213, v151
	v_add_f32_e32 v213, v213, v153
	v_add_f32_e32 v213, v213, v155
	v_add_f32_e32 v213, v213, v157
	v_add_f32_e32 v213, v213, v159
	v_fma_f32 v213, v213, v228, -v159
	v_add_f32_e32 v220, v130, v132
	v_add_f32_e32 v220, v220, v134
	v_add_f32_e32 v220, v220, v136
	v_add_f32_e32 v220, v220, v138
	v_add_f32_e32 v220, v220, v140
	v_add_f32_e32 v220, v220, v142
	v_add_f32_e32 v220, v220, v144
	v_add_f32_e32 v220, v220, v146
	v_add_f32_e32 v220, v220, v148
	v_add_f32_e32 v220, v220, v150
	v_add_f32_e32 v220, v220, v152
	v_add_f32_e32 v220, v220, v154
	v_add_f32_e32 v220, v220, v156
	v_add_f32_e32 v220, v220, v158
	v_add_f32_e32 v220, v220, v160
	v_fma_f32 v220, v220, v229, -v160
	v_add_f32_e32 v221, v131, v133
	v_add_f32_e32 v221, v221, v135
	v_add_f32_e32 v221, v221, v137
	v_add_f32_e32 v221, v221, v139
	v_add_f32_e32 v221, v221, v141
	v_add_f32_e32 v221, v221, v143
	v_add_f32_e32 v221, v221, v145
	v_add_f32_e32 v221, v221, v147
	v_add_f32_e32 v221, v221, v149
	v_add_f32_e32 v221, v221, v151
; __device__ __forceinline__ unsigned pk2(float lo, float hi) { return pg8::cvt_pk_bf16(lo, hi); }
; __device__ __forceinline__ void unpack8(const v4u w, float (&f)[8]) { f[0] = bflo(w.x); f[1] = bfhi(w.x); f[2] = bflo(w.y); f[3] = bfhi(w.y); f[4] = bflo(w.z); f[5] = bfhi(w.z); f[6] = bflo(w.w); f[7] = bfhi(w.w); }
; template <int W> __device__ __forceinline__ void pool_item(Frame& F, int row, int t, int c8) {
;     float s[8], u[8];
; #pragma unroll
;     for (int i = 0; i < 8; ++i) s[i] = 0.f;
;     v4u ld[W];
; #pragma unroll
;     for (int k = 0; k < W; ++k) { const int kk = (t - k) >= 0 ? k : t; ld[k] = *(const v4u*)(F.PROJ + (size_t)(row - kk) * INWP + O_UPOOL + c8); }
; #pragma unroll
;     for (int k = W - 1; k >= 0; --k) { unpack8(ld[k], u); const float wgt = (t - k) >= 0 ? 1.f : 0.f;
; #pragma unroll
;         for (int i = 0; i < 8; ++i) s[i] += wgt * u[i]; }
;     const int cnt = (t + 1) < W ? (t + 1) : W;
;     const float inv = 1.0f / (float)cnt;
;     v4u o; o.x = pk2(s[0] * inv - u[0], s[1] * inv - u[1]); o.y = pk2(s[2] * inv - u[2], s[3] * inv - u[3]); o.z = pk2(s[4] * inv - u[4], s[5] * inv - u[5]); o.w = pk2(s[6] * inv - u[6], s[7] * inv - u[7]);
;     *(v4u*)(F.Y + (size_t)row * 1024 + c8) = o;
; }
	v_add_f32_e32 v221, v221, v153
	v_add_f32_e32 v221, v221, v155
	v_add_f32_e32 v221, v221, v157
	v_add_f32_e32 v221, v221, v159
	v_add_f32_e32 v221, v221, v161
	v_fma_f32 v221, v221, v229, -v161
	v_lshlrev_b32_e32 v124, 16, v50
	v_and_b32_e32 v125, 0xffff0000, v50
	v_lshlrev_b32_e32 v126, 16, v54
	v_and_b32_e32 v127, 0xffff0000, v54
	v_lshlrev_b32_e32 v128, 16, v58
	v_and_b32_e32 v129, 0xffff0000, v58
	v_lshlrev_b32_e32 v130, 16, v62
	v_and_b32_e32 v131, 0xffff0000, v62
	v_lshlrev_b32_e32 v132, 16, v66
	v_and_b32_e32 v133, 0xffff0000, v66
	v_lshlrev_b32_e32 v134, 16, v70
	v_and_b32_e32 v135, 0xffff0000, v70
	v_lshlrev_b32_e32 v136, 16, v74
	v_and_b32_e32 v137, 0xffff0000, v74
	v_lshlrev_b32_e32 v138, 16, v78
	v_and_b32_e32 v139, 0xffff0000, v78
	v_lshlrev_b32_e32 v140, 16, v82
	v_and_b32_e32 v141, 0xffff0000, v82
	v_lshlrev_b32_e32 v142, 16, v86
	v_and_b32_e32 v143, 0xffff0000, v86
	v_lshlrev_b32_e32 v144, 16, v90
	v_and_b32_e32 v145, 0xffff0000, v90
	v_lshlrev_b32_e32 v146, 16, v94
	v_and_b32_e32 v147, 0xffff0000, v94
	v_lshlrev_b32_e32 v148, 16, v98
	v_and_b32_e32 v149, 0xffff0000, v98
	v_lshlrev_b32_e32 v150, 16, v102
	v_and_b32_e32 v151, 0xffff0000, v102
	v_lshlrev_b32_e32 v152, 16, v106
	v_and_b32_e32 v153, 0xffff0000, v106
	v_lshlrev_b32_e32 v154, 16, v110
	v_and_b32_e32 v155, 0xffff0000, v110
	v_lshlrev_b32_e32 v156, 16, v114
	v_and_b32_e32 v157, 0xffff0000, v114
	v_lshlrev_b32_e32 v158, 16, v118
	v_and_b32_e32 v159, 0xffff0000, v118
	v_lshlrev_b32_e32 v160, 16, v122
	v_and_b32_e32 v161, 0xffff0000, v122
	v_add_f32_e32 v198, v124, v126
	v_add_f32_e32 v198, v198, v128
	v_add_f32_e32 v198, v198, v130
	v_add_f32_e32 v198, v198, v132
	v_add_f32_e32 v198, v198, v134
	v_add_f32_e32 v198, v198, v136
	v_add_f32_e32 v198, v198, v138
	v_add_f32_e32 v198, v198, v140
	v_add_f32_e32 v198, v198, v142
	v_add_f32_e32 v198, v198, v144
	v_add_f32_e32 v198, v198, v146
	v_add_f32_e32 v198, v198, v148
	v_add_f32_e32 v198, v198, v150
	v_add_f32_e32 v198, v198, v152
	v_add_f32_e32 v198, v198, v154
	v_fma_f32 v198, v198, v226, -v154
	v_add_f32_e32 v199, v125, v127
	v_add_f32_e32 v199, v199, v129
	v_add_f32_e32 v199, v199, v131
	v_add_f32_e32 v199, v199, v133
	v_add_f32_e32 v199, v199, v135
	v_add_f32_e32 v199, v199, v137
	v_add_f32_e32 v199, v199, v139
	v_add_f32_e32 v199, v199, v141
	v_add_f32_e32 v199, v199, v143
	v_add_f32_e32 v199, v199, v145
	v_add_f32_e32 v199, v199, v147
	v_add_f32_e32 v199, v199, v149
	v_add_f32_e32 v199, v199, v151
	v_add_f32_e32 v199, v199, v153
	v_add_f32_e32 v199, v199, v155
	v_fma_f32 v199, v199, v226, -v155
	v_add_f32_e32 v206, v126, v128
	v_add_f32_e32 v206, v206, v130
	v_add_f32_e32 v206, v206, v132
	v_add_f32_e32 v206, v206, v134
	v_add_f32_e32 v206, v206, v136
	v_add_f32_e32 v206, v206, v138
	v_add_f32_e32 v206, v206, v140
	v_add_f32_e32 v206, v206, v142
	v_add_f32_e32 v206, v206, v144
	v_add_f32_e32 v206, v206, v146
	v_add_f32_e32 v206, v206, v148
	v_add_f32_e32 v206, v206, v150
	v_add_f32_e32 v206, v206, v152
	v_add_f32_e32 v206, v206, v154
	v_add_f32_e32 v206, v206, v156
	v_fma_f32 v206, v206, v227, -v156
	v_add_f32_e32 v207, v127, v129
	v_add_f32_e32 v207, v207, v131
	v_add_f32_e32 v207, v207, v133
	v_add_f32_e32 v207, v207, v135
	v_add_f32_e32 v207, v207, v137
	v_add_f32_e32 v207, v207, v139
	v_add_f32_e32 v207, v207, v141
	v_add_f32_e32 v207, v207, v143
	v_add_f32_e32 v207, v207, v145
	v_add_f32_e32 v207, v207, v147
	v_add_f32_e32 v207, v207, v149
	v_add_f32_e32 v207, v207, v151
	v_add_f32_e32 v207, v207, v153
	v_add_f32_e32 v207, v207, v155
	v_add_f32_e32 v207, v207, v157
	v_fma_f32 v207, v207, v227, -v157
	v_add_f32_e32 v214, v128, v130
	v_add_f32_e32 v214, v214, v132
	v_add_f32_e32 v214, v214, v134
	v_add_f32_e32 v214, v214, v136
	v_add_f32_e32 v214, v214, v138
	v_add_f32_e32 v214, v214, v140
	v_add_f32_e32 v214, v214, v142
	v_add_f32_e32 v214, v214, v144
	v_add_f32_e32 v214, v214, v146
	v_add_f32_e32 v214, v214, v148
	v_add_f32_e32 v214, v214, v150
	v_add_f32_e32 v214, v214, v152
	v_add_f32_e32 v214, v214, v154
	v_add_f32_e32 v214, v214, v156
	v_add_f32_e32 v214, v214, v158
	v_fma_f32 v214, v214, v228, -v158
	v_add_f32_e32 v215, v129, v131
	v_add_f32_e32 v215, v215, v133
	v_add_f32_e32 v215, v215, v135
	v_add_f32_e32 v215, v215, v137
	v_add_f32_e32 v215, v215, v139
	v_add_f32_e32 v215, v215, v141
	v_add_f32_e32 v215, v215, v143
	v_add_f32_e32 v215, v215, v145
	v_add_f32_e32 v215, v215, v147
	v_add_f32_e32 v215, v215, v149
	v_add_f32_e32 v215, v215, v151
	v_add_f32_e32 v215, v215, v153
	v_add_f32_e32 v215, v215, v155
	v_add_f32_e32 v215, v215, v157
	v_add_f32_e32 v215, v215, v159
	v_fma_f32 v215, v215, v228, -v159
	v_add_f32_e32 v222, v130, v132
	v_add_f32_e32 v222, v222, v134
	v_add_f32_e32 v222, v222, v136
	v_add_f32_e32 v222, v222, v138
	v_add_f32_e32 v222, v222, v140
	v_add_f32_e32 v222, v222, v142
	v_add_f32_e32 v222, v222, v144
	v_add_f32_e32 v222, v222, v146
	v_add_f32_e32 v222, v222, v148
	v_add_f32_e32 v222, v222, v150
	v_add_f32_e32 v222, v222, v152
	v_add_f32_e32 v222, v222, v154
	v_add_f32_e32 v222, v222, v156
	v_add_f32_e32 v222, v222, v158
	v_add_f32_e32 v222, v222, v160
	v_fma_f32 v222, v222, v229, -v160
	v_add_f32_e32 v223, v131, v133
	v_add_f32_e32 v223, v223, v135
	v_add_f32_e32 v223, v223, v137
	v_add_f32_e32 v223, v223, v139
	v_add_f32_e32 v223, v223, v141
	v_add_f32_e32 v223, v223, v143
	v_add_f32_e32 v223, v223, v145
	v_add_f32_e32 v223, v223, v147
	v_add_f32_e32 v223, v223, v149
	v_add_f32_e32 v223, v223, v151
	v_add_f32_e32 v223, v223, v153
	v_add_f32_e32 v223, v223, v155
	v_add_f32_e32 v223, v223, v157
	v_add_f32_e32 v223, v223, v159
	v_add_f32_e32 v223, v223, v161
	v_fma_f32 v223, v223, v229, -v161
; __device__ __forceinline__ unsigned pk2(float lo, float hi) { return pg8::cvt_pk_bf16(lo, hi); }
; __device__ __forceinline__ void unpack8(const v4u w, float (&f)[8]) { f[0] = bflo(w.x); f[1] = bfhi(w.x); f[2] = bflo(w.y); f[3] = bfhi(w.y); f[4] = bflo(w.z); f[5] = bfhi(w.z); f[6] = bflo(w.w); f[7] = bfhi(w.w); }
; template <int W> __device__ __forceinline__ void pool_item(Frame& F, int row, int t, int c8) {
;     float s[8], u[8];
; #pragma unroll
;     for (int i = 0; i < 8; ++i) s[i] = 0.f;
;     v4u ld[W];
; #pragma unroll
;     for (int k = 0; k < W; ++k) { const int kk = (t - k) >= 0 ? k : t; ld[k] = *(const v4u*)(F.PROJ + (size_t)(row - kk) * INWP + O_UPOOL + c8); }
; #pragma unroll
;     for (int k = W - 1; k >= 0; --k) { unpack8(ld[k], u); const float wgt = (t - k) >= 0 ? 1.f : 0.f;
; #pragma unroll
;         for (int i = 0; i < 8; ++i) s[i] += wgt * u[i]; }
;     const int cnt = (t + 1) < W ? (t + 1) : W;
;     const float inv = 1.0f / (float)cnt;
;     v4u o; o.x = pk2(s[0] * inv - u[0], s[1] * inv - u[1]); o.y = pk2(s[2] * inv - u[2], s[3] * inv - u[3]); o.z = pk2(s[4] * inv - u[4], s[5] * inv - u[5]); o.w = pk2(s[6] * inv - u[6], s[7] * inv - u[7]);
;     *(v4u*)(F.Y + (size_t)row * 1024 + c8) = o;
; }
	v_lshlrev_b32_e32 v124, 16, v51
	v_and_b32_e32 v125, 0xffff0000, v51
	v_lshlrev_b32_e32 v126, 16, v55
	v_and_b32_e32 v127, 0xffff0000, v55
	v_lshlrev_b32_e32 v128, 16, v59
	v_and_b32_e32 v129, 0xffff0000, v59
	v_lshlrev_b32_e32 v130, 16, v63
	v_and_b32_e32 v131, 0xffff0000, v63
	v_lshlrev_b32_e32 v132, 16, v67
	v_and_b32_e32 v133, 0xffff0000, v67
	v_lshlrev_b32_e32 v134, 16, v71
	v_and_b32_e32 v135, 0xffff0000, v71
	v_lshlrev_b32_e32 v136, 16, v75
	v_and_b32_e32 v137, 0xffff0000, v75
	v_lshlrev_b32_e32 v138, 16, v79
	v_and_b32_e32 v139, 0xffff0000, v79
	v_lshlrev_b32_e32 v140, 16, v83
	v_and_b32_e32 v141, 0xffff0000, v83
	v_lshlrev_b32_e32 v142, 16, v87
	v_and_b32_e32 v143, 0xffff0000, v87
	v_lshlrev_b32_e32 v144, 16, v91
	v_and_b32_e32 v145, 0xffff0000, v91
	v_lshlrev_b32_e32 v146, 16, v95
	v_and_b32_e32 v147, 0xffff0000, v95
	v_lshlrev_b32_e32 v148, 16, v99
	v_and_b32_e32 v149, 0xffff0000, v99
	v_lshlrev_b32_e32 v150, 16, v103
	v_and_b32_e32 v151, 0xffff0000, v103
	v_lshlrev_b32_e32 v152, 16, v107
	v_and_b32_e32 v153, 0xffff0000, v107
	v_lshlrev_b32_e32 v154, 16, v111
	v_and_b32_e32 v155, 0xffff0000, v111
	v_lshlrev_b32_e32 v156, 16, v115
	v_and_b32_e32 v157, 0xffff0000, v115
	v_lshlrev_b32_e32 v158, 16, v119
	v_and_b32_e32 v159, 0xffff0000, v119
	v_lshlrev_b32_e32 v160, 16, v123
	v_and_b32_e32 v161, 0xffff0000, v123
	v_add_f32_e32 v200, v124, v126
	v_add_f32_e32 v200, v200, v128
	v_add_f32_e32 v200, v200, v130
	v_add_f32_e32 v200, v200, v132
	v_add_f32_e32 v200, v200, v134
	v_add_f32_e32 v200, v200, v136
	v_add_f32_e32 v200, v200, v138
	v_add_f32_e32 v200, v200, v140
	v_add_f32_e32 v200, v200, v142
	v_add_f32_e32 v200, v200, v144
	v_add_f32_e32 v200, v200, v146
	v_add_f32_e32 v200, v200, v148
	v_add_f32_e32 v200, v200, v150
	v_add_f32_e32 v200, v200, v152
	v_add_f32_e32 v200, v200, v154
	v_fma_f32 v200, v200, v226, -v154
	v_add_f32_e32 v201, v125, v127
	v_add_f32_e32 v201, v201, v129
	v_add_f32_e32 v201, v201, v131
	v_add_f32_e32 v201, v201, v133
	v_add_f32_e32 v201, v201, v135
	v_add_f32_e32 v201, v201, v137
	v_add_f32_e32 v201, v201, v139
	v_add_f32_e32 v201, v201, v141
	v_add_f32_e32 v201, v201, v143
	v_add_f32_e32 v201, v201, v145
	v_add_f32_e32 v201, v201, v147
	v_add_f32_e32 v201, v201, v149
	v_add_f32_e32 v201, v201, v151
	v_add_f32_e32 v201, v201, v153
	v_add_f32_e32 v201, v201, v155
	v_fma_f32 v201, v201, v226, -v155
	v_add_f32_e32 v208, v126, v128
	v_add_f32_e32 v208, v208, v130
	v_add_f32_e32 v208, v208, v132
	v_add_f32_e32 v208, v208, v134
	v_add_f32_e32 v208, v208, v136
	v_add_f32_e32 v208, v208, v138
	v_add_f32_e32 v208, v208, v140
	v_add_f32_e32 v208, v208, v142
	v_add_f32_e32 v208, v208, v144
	v_add_f32_e32 v208, v208, v146
	v_add_f32_e32 v208, v208, v148
	v_add_f32_e32 v208, v208, v150
	v_add_f32_e32 v208, v208, v152
	v_add_f32_e32 v208, v208, v154
	v_add_f32_e32 v208, v208, v156
	v_fma_f32 v208, v208, v227, -v156
	v_add_f32_e32 v209, v127, v129
	v_add_f32_e32 v209, v209, v131
	v_add_f32_e32 v209, v209, v133
	v_add_f32_e32 v209, v209, v135
	v_add_f32_e32 v209, v209, v137
	v_add_f32_e32 v209, v209, v139
	v_add_f32_e32 v209, v209, v141
	v_add_f32_e32 v209, v209, v143
	v_add_f32_e32 v209, v209, v145
	v_add_f32_e32 v209, v209, v147
	v_add_f32_e32 v209, v209, v149
	v_add_f32_e32 v209, v209, v151
	v_add_f32_e32 v209, v209, v153
	v_add_f32_e32 v209, v209, v155
	v_add_f32_e32 v209, v209, v157
	v_fma_f32 v209, v209, v227, -v157
	v_add_f32_e32 v216, v128, v130
	v_add_f32_e32 v216, v216, v132
	v_add_f32_e32 v216, v216, v134
	v_add_f32_e32 v216, v216, v136
	v_add_f32_e32 v216, v216, v138
	v_add_f32_e32 v216, v216, v140
	v_add_f32_e32 v216, v216, v142
	v_add_f32_e32 v216, v216, v144
	v_add_f32_e32 v216, v216, v146
	v_add_f32_e32 v216, v216, v148
	v_add_f32_e32 v216, v216, v150
	v_add_f32_e32 v216, v216, v152
	v_add_f32_e32 v216, v216, v154
	v_add_f32_e32 v216, v216, v156
	v_add_f32_e32 v216, v216, v158
	v_fma_f32 v216, v216, v228, -v158
	v_add_f32_e32 v217, v129, v131
	v_add_f32_e32 v217, v217, v133
	v_add_f32_e32 v217, v217, v135
	v_add_f32_e32 v217, v217, v137
	v_add_f32_e32 v217, v217, v139
	v_add_f32_e32 v217, v217, v141
	v_add_f32_e32 v217, v217, v143
	v_add_f32_e32 v217, v217, v145
	v_add_f32_e32 v217, v217, v147
	v_add_f32_e32 v217, v217, v149
	v_add_f32_e32 v217, v217, v151
	v_add_f32_e32 v217, v217, v153
	v_add_f32_e32 v217, v217, v155
	v_add_f32_e32 v217, v217, v157
	v_add_f32_e32 v217, v217, v159
	v_fma_f32 v217, v217, v228, -v159
	v_add_f32_e32 v224, v130, v132
	v_add_f32_e32 v224, v224, v134
	v_add_f32_e32 v224, v224, v136
	v_add_f32_e32 v224, v224, v138
	v_add_f32_e32 v224, v224, v140
	v_add_f32_e32 v224, v224, v142
	v_add_f32_e32 v224, v224, v144
	v_add_f32_e32 v224, v224, v146
	v_add_f32_e32 v224, v224, v148
	v_add_f32_e32 v224, v224, v150
	v_add_f32_e32 v224, v224, v152
	v_add_f32_e32 v224, v224, v154
	v_add_f32_e32 v224, v224, v156
	v_add_f32_e32 v224, v224, v158
	v_add_f32_e32 v224, v224, v160
	v_fma_f32 v224, v224, v229, -v160
	v_add_f32_e32 v225, v131, v133
	v_add_f32_e32 v225, v225, v135
	v_add_f32_e32 v225, v225, v137
	v_add_f32_e32 v225, v225, v139
	v_add_f32_e32 v225, v225, v141
	v_add_f32_e32 v225, v225, v143
	v_add_f32_e32 v225, v225, v145
	v_add_f32_e32 v225, v225, v147
	v_add_f32_e32 v225, v225, v149
	v_add_f32_e32 v225, v225, v151
	v_add_f32_e32 v225, v225, v153
	v_add_f32_e32 v225, v225, v155
	v_add_f32_e32 v225, v225, v157
	v_add_f32_e32 v225, v225, v159
	v_add_f32_e32 v225, v225, v161
	v_fma_f32 v225, v225, v229, -v161
	v_cvt_pk_bf16_f32 v194, v194, v195
	v_cvt_pk_bf16_f32 v195, v196, v197
	v_cvt_pk_bf16_f32 v196, v198, v199
	v_cvt_pk_bf16_f32 v197, v200, v201
	global_store_dwordx4 v17, v[194:197], s[14:15] nt
	v_cvt_pk_bf16_f32 v202, v202, v203
	v_cvt_pk_bf16_f32 v203, v204, v205
	v_cvt_pk_bf16_f32 v204, v206, v207
	v_cvt_pk_bf16_f32 v205, v208, v209
	v_add_u32_e32 v13, 0x800, v17
	global_store_dwordx4 v13, v[202:205], s[14:15] nt
	v_cvt_pk_bf16_f32 v210, v210, v211
	v_cvt_pk_bf16_f32 v211, v212, v213
	v_cvt_pk_bf16_f32 v212, v214, v215
	v_cvt_pk_bf16_f32 v213, v216, v217
	v_add_u32_e32 v13, 0x1000, v17
	global_store_dwordx4 v13, v[210:213], s[14:15] nt
	v_cvt_pk_bf16_f32 v218, v218, v219
	v_cvt_pk_bf16_f32 v219, v220, v221
	v_cvt_pk_bf16_f32 v220, v222, v223
	v_cvt_pk_bf16_f32 v221, v224, v225
	v_add_u32_e32 v13, 0x1800, v17
	global_store_dwordx4 v13, v[218:221], s[14:15] nt
	s_branch .Lpc_conv
; __device__ __forceinline__ unsigned pk2(float lo, float hi) { return pg8::cvt_pk_bf16(lo, hi); }
; __device__ __forceinline__ void unpack8(const v4u w, float (&f)[8]) { f[0] = bflo(w.x); f[1] = bfhi(w.x); f[2] = bflo(w.y); f[3] = bfhi(w.y); f[4] = bflo(w.z); f[5] = bfhi(w.z); f[6] = bflo(w.w); f[7] = bfhi(w.w); }
; template <int W> __device__ __forceinline__ void pool_item(Frame& F, int row, int t, int c8) {
;     float s[8], u[8];
; #pragma unroll
;     for (int i = 0; i < 8; ++i) s[i] = 0.f;
;     v4u ld[W];
; #pragma unroll
;     for (int k = 0; k < W; ++k) { const int kk = (t - k) >= 0 ? k : t; ld[k] = *(const v4u*)(F.PROJ + (size_t)(row - kk) * INWP + O_UPOOL + c8); }
; #pragma unroll
;     for (int k = W - 1; k >= 0; --k) { unpack8(ld[k], u); const float wgt = (t - k) >= 0 ? 1.f : 0.f;
; #pragma unroll
;         for (int i = 0; i < 8; ++i) s[i] += wgt * u[i]; }
;     const int cnt = (t + 1) < W ? (t + 1) : W;
;     const float inv = 1.0f / (float)cnt;
;     v4u o; o.x = pk2(s[0] * inv - u[0], s[1] * inv - u[1]); o.y = pk2(s[2] * inv - u[2], s[3] * inv - u[3]); o.z = pk2(s[4] * inv - u[4], s[5] * inv - u[5]); o.w = pk2(s[6] * inv - u[6], s[7] * inv - u[7]);
;     *(v4u*)(F.Y + (size_t)row * 1024 + c8) = o;
; }
.Lpc_g1:
	v_add_u32_e32 v14, 0x200, v7
	v_add_u32_e32 v15, 0x400, v7
	v_add_u32_e32 v16, 0x200, v9
	v_add_u32_e32 v17, 0x400, v9
	v_min_u32_e32 v11, 0xa200, v6
	v_sub_u32_e32 v12, v14, v11
	global_load_dwordx4 v[20:23], v12, s[96:97] nt
	v_min_u32_e32 v11, 0x6c00, v6
	v_sub_u32_e32 v12, v14, v11
	global_load_dwordx4 v[24:27], v12, s[96:97] nt
	v_min_u32_e32 v11, 0x3600, v6
	v_sub_u32_e32 v12, v14, v11
	global_load_dwordx4 v[28:31], v12, s[96:97] nt
	global_load_dwordx4 v[32:35], v14, s[96:97] nt
	v_add_u32_e32 v12, 0x3600, v14
	global_load_dwordx4 v[36:39], v12, s[96:97] nt
	v_add_u32_e32 v12, 0x6c00, v14
	global_load_dwordx4 v[40:43], v12, s[96:97] nt
	v_add_u32_e32 v12, 0xa200, v14
	global_load_dwordx4 v[44:47], v12, s[96:97] nt
	v_min_u32_e32 v11, 0x17a00, v6
	v_sub_u32_e32 v12, v15, v11
	global_load_dwordx4 v[48:51], v12, s[96:97] nt
	v_min_u32_e32 v11, 0x14400, v6
	v_sub_u32_e32 v12, v15, v11
	global_load_dwordx4 v[52:55], v12, s[96:97] nt
	v_min_u32_e32 v11, 0x10e00, v6
	v_sub_u32_e32 v12, v15, v11
	global_load_dwordx4 v[56:59], v12, s[96:97] nt
	v_min_u32_e32 v11, 0xd800, v6
	v_sub_u32_e32 v12, v15, v11
	global_load_dwordx4 v[60:63], v12, s[96:97] nt
	v_min_u32_e32 v11, 0xa200, v6
	v_sub_u32_e32 v12, v15, v11
	global_load_dwordx4 v[64:67], v12, s[96:97] nt
	v_min_u32_e32 v11, 0x6c00, v6
	v_sub_u32_e32 v12, v15, v11
	global_load_dwordx4 v[68:71], v12, s[96:97] nt
	v_min_u32_e32 v11, 0x3600, v6
	v_sub_u32_e32 v12, v15, v11
	global_load_dwordx4 v[72:75], v12, s[96:97] nt
	global_load_dwordx4 v[76:79], v15, s[96:97] nt
	v_add_u32_e32 v12, 0x3600, v15
	global_load_dwordx4 v[80:83], v12, s[96:97] nt
	v_add_u32_e32 v12, 0x6c00, v15
	global_load_dwordx4 v[84:87], v12, s[96:97] nt
	v_add_u32_e32 v12, 0xa200, v15
	global_load_dwordx4 v[88:91], v12, s[96:97] nt
	s_waitcnt vmcnt(11)
	v_cmp_le_u32_e32 vcc, 3, v5
	s_nop 1
	v_cndmask_b32_e32 v20, 0, v20, vcc
	v_cndmask_b32_e32 v21, 0, v21, vcc
	v_cndmask_b32_e32 v22, 0, v22, vcc
	v_cndmask_b32_e32 v23, 0, v23, vcc
	v_cmp_le_u32_e32 vcc, 2, v5
	s_nop 1
	v_cndmask_b32_e32 v24, 0, v24, vcc
	v_cndmask_b32_e32 v25, 0, v25, vcc
	v_cndmask_b32_e32 v26, 0, v26, vcc
	v_cndmask_b32_e32 v27, 0, v27, vcc
	v_cmp_le_u32_e32 vcc, 1, v5
	s_nop 1
	v_cndmask_b32_e32 v28, 0, v28, vcc
	v_cndmask_b32_e32 v29, 0, v29, vcc
	v_cndmask_b32_e32 v30, 0, v30, vcc
	v_cndmask_b32_e32 v31, 0, v31, vcc
	v_add_u32_e32 v226, 1, v5
	v_min_u32_e32 v226, 4, v226
	v_cvt_f32_u32_e32 v226, v226
	v_rcp_f32_e32 v226, v226
	v_add_u32_e32 v227, 2, v5
	v_min_u32_e32 v227, 4, v227
	v_cvt_f32_u32_e32 v227, v227
	v_rcp_f32_e32 v227, v227
	v_add_u32_e32 v228, 3, v5
	v_min_u32_e32 v228, 4, v228
	v_cvt_f32_u32_e32 v228, v228
	v_rcp_f32_e32 v228, v228
	v_add_u32_e32 v229, 4, v5
	v_min_u32_e32 v229, 4, v229
	v_cvt_f32_u32_e32 v229, v229
	v_rcp_f32_e32 v229, v229
	v_lshlrev_b32_e32 v124, 16, v20
	v_and_b32_e32 v125, 0xffff0000, v20
	v_lshlrev_b32_e32 v126, 16, v24
	v_and_b32_e32 v127, 0xffff0000, v24
	v_lshlrev_b32_e32 v128, 16, v28
	v_and_b32_e32 v129, 0xffff0000, v28
	v_lshlrev_b32_e32 v130, 16, v32
	v_and_b32_e32 v131, 0xffff0000, v32
	v_lshlrev_b32_e32 v132, 16, v36
	v_and_b32_e32 v133, 0xffff0000, v36
	v_lshlrev_b32_e32 v134, 16, v40
	v_and_b32_e32 v135, 0xffff0000, v40
	v_lshlrev_b32_e32 v136, 16, v44
	v_and_b32_e32 v137, 0xffff0000, v44
	v_add_f32_e32 v194, v124, v126
	v_add_f32_e32 v194, v194, v128
	v_add_f32_e32 v194, v194, v130
	v_fma_f32 v194, v194, v226, -v130
	v_add_f32_e32 v195, v125, v127
	v_add_f32_e32 v195, v195, v129
	v_add_f32_e32 v195, v195, v131
	v_fma_f32 v195, v195, v226, -v131
	v_add_f32_e32 v202, v126, v128
	v_add_f32_e32 v202, v202, v130
	v_add_f32_e32 v202, v202, v132
	v_fma_f32 v202, v202, v227, -v132
	v_add_f32_e32 v203, v127, v129
	v_add_f32_e32 v203, v203, v131
	v_add_f32_e32 v203, v203, v133
	v_fma_f32 v203, v203, v227, -v133
	v_add_f32_e32 v210, v128, v130
	v_add_f32_e32 v210, v210, v132
	v_add_f32_e32 v210, v210, v134
	v_fma_f32 v210, v210, v228, -v134
	v_add_f32_e32 v211, v129, v131
	v_add_f32_e32 v211, v211, v133
	v_add_f32_e32 v211, v211, v135
	v_fma_f32 v211, v211, v228, -v135
	v_add_f32_e32 v218, v130, v132
	v_add_f32_e32 v218, v218, v134
	v_add_f32_e32 v218, v218, v136
	v_fma_f32 v218, v218, v229, -v136
	v_add_f32_e32 v219, v131, v133
	v_add_f32_e32 v219, v219, v135
	v_add_f32_e32 v219, v219, v137
	v_fma_f32 v219, v219, v229, -v137
	v_lshlrev_b32_e32 v124, 16, v21
	v_and_b32_e32 v125, 0xffff0000, v21
	v_lshlrev_b32_e32 v126, 16, v25
	v_and_b32_e32 v127, 0xffff0000, v25
	v_lshlrev_b32_e32 v128, 16, v29
	v_and_b32_e32 v129, 0xffff0000, v29
	v_lshlrev_b32_e32 v130, 16, v33
	v_and_b32_e32 v131, 0xffff0000, v33
	v_lshlrev_b32_e32 v132, 16, v37
	v_and_b32_e32 v133, 0xffff0000, v37
	v_lshlrev_b32_e32 v134, 16, v41
	v_and_b32_e32 v135, 0xffff0000, v41
	v_lshlrev_b32_e32 v136, 16, v45
	v_and_b32_e32 v137, 0xffff0000, v45
	v_add_f32_e32 v196, v124, v126
	v_add_f32_e32 v196, v196, v128
	v_add_f32_e32 v196, v196, v130
	v_fma_f32 v196, v196, v226, -v130
	v_add_f32_e32 v197, v125, v127
	v_add_f32_e32 v197, v197, v129
	v_add_f32_e32 v197, v197, v131
	v_fma_f32 v197, v197, v226, -v131
	v_add_f32_e32 v204, v126, v128
	v_add_f32_e32 v204, v204, v130
	v_add_f32_e32 v204, v204, v132
	v_fma_f32 v204, v204, v227, -v132
	v_add_f32_e32 v205, v127, v129
	v_add_f32_e32 v205, v205, v131
	v_add_f32_e32 v205, v205, v133
	v_fma_f32 v205, v205, v227, -v133
	v_add_f32_e32 v212, v128, v130
	v_add_f32_e32 v212, v212, v132
	v_add_f32_e32 v212, v212, v134
	v_fma_f32 v212, v212, v228, -v134
	v_add_f32_e32 v213, v129, v131
	v_add_f32_e32 v213, v213, v133
	v_add_f32_e32 v213, v213, v135
	v_fma_f32 v213, v213, v228, -v135
	v_add_f32_e32 v220, v130, v132
; __device__ __forceinline__ unsigned pk2(float lo, float hi) { return pg8::cvt_pk_bf16(lo, hi); }
; __device__ __forceinline__ void unpack8(const v4u w, float (&f)[8]) { f[0] = bflo(w.x); f[1] = bfhi(w.x); f[2] = bflo(w.y); f[3] = bfhi(w.y); f[4] = bflo(w.z); f[5] = bfhi(w.z); f[6] = bflo(w.w); f[7] = bfhi(w.w); }
; template <int W> __device__ __forceinline__ void pool_item(Frame& F, int row, int t, int c8) {
;     float s[8], u[8];
; #pragma unroll
;     for (int i = 0; i < 8; ++i) s[i] = 0.f;
;     v4u ld[W];
; #pragma unroll
;     for (int k = 0; k < W; ++k) { const int kk = (t - k) >= 0 ? k : t; ld[k] = *(const v4u*)(F.PROJ + (size_t)(row - kk) * INWP + O_UPOOL + c8); }
; #pragma unroll
;     for (int k = W - 1; k >= 0; --k) { unpack8(ld[k], u); const float wgt = (t - k) >= 0 ? 1.f : 0.f;
; #pragma unroll
;         for (int i = 0; i < 8; ++i) s[i] += wgt * u[i]; }
;     const int cnt = (t + 1) < W ? (t + 1) : W;
;     const float inv = 1.0f / (float)cnt;
;     v4u o; o.x = pk2(s[0] * inv - u[0], s[1] * inv - u[1]); o.y = pk2(s[2] * inv - u[2], s[3] * inv - u[3]); o.z = pk2(s[4] * inv - u[4], s[5] * inv - u[5]); o.w = pk2(s[6] * inv - u[6], s[7] * inv - u[7]);
;     *(v4u*)(F.Y + (size_t)row * 1024 + c8) = o;
; }
	v_add_f32_e32 v220, v220, v134
	v_add_f32_e32 v220, v220, v136
	v_fma_f32 v220, v220, v229, -v136
	v_add_f32_e32 v221, v131, v133
	v_add_f32_e32 v221, v221, v135
	v_add_f32_e32 v221, v221, v137
	v_fma_f32 v221, v221, v229, -v137
	v_lshlrev_b32_e32 v124, 16, v22
	v_and_b32_e32 v125, 0xffff0000, v22
	v_lshlrev_b32_e32 v126, 16, v26
	v_and_b32_e32 v127, 0xffff0000, v26
	v_lshlrev_b32_e32 v128, 16, v30
	v_and_b32_e32 v129, 0xffff0000, v30
	v_lshlrev_b32_e32 v130, 16, v34
	v_and_b32_e32 v131, 0xffff0000, v34
	v_lshlrev_b32_e32 v132, 16, v38
	v_and_b32_e32 v133, 0xffff0000, v38
	v_lshlrev_b32_e32 v134, 16, v42
	v_and_b32_e32 v135, 0xffff0000, v42
	v_lshlrev_b32_e32 v136, 16, v46
	v_and_b32_e32 v137, 0xffff0000, v46
	v_add_f32_e32 v198, v124, v126
	v_add_f32_e32 v198, v198, v128
	v_add_f32_e32 v198, v198, v130
	v_fma_f32 v198, v198, v226, -v130
	v_add_f32_e32 v199, v125, v127
	v_add_f32_e32 v199, v199, v129
	v_add_f32_e32 v199, v199, v131
	v_fma_f32 v199, v199, v226, -v131
	v_add_f32_e32 v206, v126, v128
	v_add_f32_e32 v206, v206, v130
	v_add_f32_e32 v206, v206, v132
	v_fma_f32 v206, v206, v227, -v132
	v_add_f32_e32 v207, v127, v129
	v_add_f32_e32 v207, v207, v131
	v_add_f32_e32 v207, v207, v133
	v_fma_f32 v207, v207, v227, -v133
	v_add_f32_e32 v214, v128, v130
	v_add_f32_e32 v214, v214, v132
	v_add_f32_e32 v214, v214, v134
	v_fma_f32 v214, v214, v228, -v134
	v_add_f32_e32 v215, v129, v131
	v_add_f32_e32 v215, v215, v133
	v_add_f32_e32 v215, v215, v135
	v_fma_f32 v215, v215, v228, -v135
	v_add_f32_e32 v222, v130, v132
	v_add_f32_e32 v222, v222, v134
	v_add_f32_e32 v222, v222, v136
	v_fma_f32 v222, v222, v229, -v136
	v_add_f32_e32 v223, v131, v133
	v_add_f32_e32 v223, v223, v135
	v_add_f32_e32 v223, v223, v137
	v_fma_f32 v223, v223, v229, -v137
	v_lshlrev_b32_e32 v124, 16, v23
	v_and_b32_e32 v125, 0xffff0000, v23
	v_lshlrev_b32_e32 v126, 16, v27
	v_and_b32_e32 v127, 0xffff0000, v27
	v_lshlrev_b32_e32 v128, 16, v31
	v_and_b32_e32 v129, 0xffff0000, v31
	v_lshlrev_b32_e32 v130, 16, v35
	v_and_b32_e32 v131, 0xffff0000, v35
	v_lshlrev_b32_e32 v132, 16, v39
	v_and_b32_e32 v133, 0xffff0000, v39
	v_lshlrev_b32_e32 v134, 16, v43
	v_and_b32_e32 v135, 0xffff0000, v43
	v_lshlrev_b32_e32 v136, 16, v47
	v_and_b32_e32 v137, 0xffff0000, v47
	v_add_f32_e32 v200, v124, v126
	v_add_f32_e32 v200, v200, v128
	v_add_f32_e32 v200, v200, v130
	v_fma_f32 v200, v200, v226, -v130
	v_add_f32_e32 v201, v125, v127
	v_add_f32_e32 v201, v201, v129
	v_add_f32_e32 v201, v201, v131
	v_fma_f32 v201, v201, v226, -v131
	v_add_f32_e32 v208, v126, v128
	v_add_f32_e32 v208, v208, v130
	v_add_f32_e32 v208, v208, v132
	v_fma_f32 v208, v208, v227, -v132
	v_add_f32_e32 v209, v127, v129
	v_add_f32_e32 v209, v209, v131
	v_add_f32_e32 v209, v209, v133
	v_fma_f32 v209, v209, v227, -v133
	v_add_f32_e32 v216, v128, v130
	v_add_f32_e32 v216, v216, v132
	v_add_f32_e32 v216, v216, v134
	v_fma_f32 v216, v216, v228, -v134
	v_add_f32_e32 v217, v129, v131
	v_add_f32_e32 v217, v217, v133
	v_add_f32_e32 v217, v217, v135
	v_fma_f32 v217, v217, v228, -v135
	v_add_f32_e32 v224, v130, v132
	v_add_f32_e32 v224, v224, v134
	v_add_f32_e32 v224, v224, v136
	v_fma_f32 v224, v224, v229, -v136
	v_add_f32_e32 v225, v131, v133
	v_add_f32_e32 v225, v225, v135
	v_add_f32_e32 v225, v225, v137
	v_fma_f32 v225, v225, v229, -v137
	v_cvt_pk_bf16_f32 v194, v194, v195
	v_cvt_pk_bf16_f32 v195, v196, v197
	v_cvt_pk_bf16_f32 v196, v198, v199
	v_cvt_pk_bf16_f32 v197, v200, v201
	global_store_dwordx4 v16, v[194:197], s[14:15] nt
	v_cvt_pk_bf16_f32 v202, v202, v203
	v_cvt_pk_bf16_f32 v203, v204, v205
	v_cvt_pk_bf16_f32 v204, v206, v207
	v_cvt_pk_bf16_f32 v205, v208, v209
	v_add_u32_e32 v13, 0x800, v16
	global_store_dwordx4 v13, v[202:205], s[14:15] nt
	v_cvt_pk_bf16_f32 v210, v210, v211
	v_cvt_pk_bf16_f32 v211, v212, v213
	v_cvt_pk_bf16_f32 v212, v214, v215
	v_cvt_pk_bf16_f32 v213, v216, v217
	v_add_u32_e32 v13, 0x1000, v16
	global_store_dwordx4 v13, v[210:213], s[14:15] nt
	v_cvt_pk_bf16_f32 v218, v218, v219
	v_cvt_pk_bf16_f32 v219, v220, v221
	v_cvt_pk_bf16_f32 v220, v222, v223
	v_cvt_pk_bf16_f32 v221, v224, v225
	v_add_u32_e32 v13, 0x1800, v16
	global_store_dwordx4 v13, v[218:221], s[14:15] nt
	s_waitcnt vmcnt(4)
	v_cmp_le_u32_e32 vcc, 7, v5
	s_nop 1
	v_cndmask_b32_e32 v48, 0, v48, vcc
	v_cndmask_b32_e32 v49, 0, v49, vcc
	v_cndmask_b32_e32 v50, 0, v50, vcc
	v_cndmask_b32_e32 v51, 0, v51, vcc
	v_cmp_le_u32_e32 vcc, 6, v5
	s_nop 1
	v_cndmask_b32_e32 v52, 0, v52, vcc
	v_cndmask_b32_e32 v53, 0, v53, vcc
	v_cndmask_b32_e32 v54, 0, v54, vcc
	v_cndmask_b32_e32 v55, 0, v55, vcc
	v_cmp_le_u32_e32 vcc, 5, v5
	s_nop 1
	v_cndmask_b32_e32 v56, 0, v56, vcc
	v_cndmask_b32_e32 v57, 0, v57, vcc
	v_cndmask_b32_e32 v58, 0, v58, vcc
	v_cndmask_b32_e32 v59, 0, v59, vcc
	v_cmp_le_u32_e32 vcc, 4, v5
	s_nop 1
	v_cndmask_b32_e32 v60, 0, v60, vcc
	v_cndmask_b32_e32 v61, 0, v61, vcc
	v_cndmask_b32_e32 v62, 0, v62, vcc
	v_cndmask_b32_e32 v63, 0, v63, vcc
	v_cmp_le_u32_e32 vcc, 3, v5
	s_nop 1
	v_cndmask_b32_e32 v64, 0, v64, vcc
	v_cndmask_b32_e32 v65, 0, v65, vcc
	v_cndmask_b32_e32 v66, 0, v66, vcc
	v_cndmask_b32_e32 v67, 0, v67, vcc
	v_cmp_le_u32_e32 vcc, 2, v5
	s_nop 1
	v_cndmask_b32_e32 v68, 0, v68, vcc
	v_cndmask_b32_e32 v69, 0, v69, vcc
	v_cndmask_b32_e32 v70, 0, v70, vcc
	v_cndmask_b32_e32 v71, 0, v71, vcc
	v_cmp_le_u32_e32 vcc, 1, v5
	s_nop 1
	v_cndmask_b32_e32 v72, 0, v72, vcc
	v_cndmask_b32_e32 v73, 0, v73, vcc
	v_cndmask_b32_e32 v74, 0, v74, vcc
	v_cndmask_b32_e32 v75, 0, v75, vcc
	v_add_u32_e32 v226, 1, v5
	v_min_u32_e32 v226, 8, v226
	v_cvt_f32_u32_e32 v226, v226
	v_rcp_f32_e32 v226, v226
	v_add_u32_e32 v227, 2, v5
	v_min_u32_e32 v227, 8, v227
; __device__ __forceinline__ unsigned pk2(float lo, float hi) { return pg8::cvt_pk_bf16(lo, hi); }
; __device__ __forceinline__ void unpack8(const v4u w, float (&f)[8]) { f[0] = bflo(w.x); f[1] = bfhi(w.x); f[2] = bflo(w.y); f[3] = bfhi(w.y); f[4] = bflo(w.z); f[5] = bfhi(w.z); f[6] = bflo(w.w); f[7] = bfhi(w.w); }
; template <int W> __device__ __forceinline__ void pool_item(Frame& F, int row, int t, int c8) {
;     float s[8], u[8];
; #pragma unroll
;     for (int i = 0; i < 8; ++i) s[i] = 0.f;
;     v4u ld[W];
; #pragma unroll
;     for (int k = 0; k < W; ++k) { const int kk = (t - k) >= 0 ? k : t; ld[k] = *(const v4u*)(F.PROJ + (size_t)(row - kk) * INWP + O_UPOOL + c8); }
; #pragma unroll
;     for (int k = W - 1; k >= 0; --k) { unpack8(ld[k], u); const float wgt = (t - k) >= 0 ? 1.f : 0.f;
; #pragma unroll
;         for (int i = 0; i < 8; ++i) s[i] += wgt * u[i]; }
;     const int cnt = (t + 1) < W ? (t + 1) : W;
;     const float inv = 1.0f / (float)cnt;
;     v4u o; o.x = pk2(s[0] * inv - u[0], s[1] * inv - u[1]); o.y = pk2(s[2] * inv - u[2], s[3] * inv - u[3]); o.z = pk2(s[4] * inv - u[4], s[5] * inv - u[5]); o.w = pk2(s[6] * inv - u[6], s[7] * inv - u[7]);
;     *(v4u*)(F.Y + (size_t)row * 1024 + c8) = o;
; }
	v_cvt_f32_u32_e32 v227, v227
	v_rcp_f32_e32 v227, v227
	v_add_u32_e32 v228, 3, v5
	v_min_u32_e32 v228, 8, v228
	v_cvt_f32_u32_e32 v228, v228
	v_rcp_f32_e32 v228, v228
	v_add_u32_e32 v229, 4, v5
	v_min_u32_e32 v229, 8, v229
	v_cvt_f32_u32_e32 v229, v229
	v_rcp_f32_e32 v229, v229
	v_lshlrev_b32_e32 v124, 16, v48
	v_and_b32_e32 v125, 0xffff0000, v48
	v_lshlrev_b32_e32 v126, 16, v52
	v_and_b32_e32 v127, 0xffff0000, v52
	v_lshlrev_b32_e32 v128, 16, v56
	v_and_b32_e32 v129, 0xffff0000, v56
	v_lshlrev_b32_e32 v130, 16, v60
	v_and_b32_e32 v131, 0xffff0000, v60
	v_lshlrev_b32_e32 v132, 16, v64
	v_and_b32_e32 v133, 0xffff0000, v64
	v_lshlrev_b32_e32 v134, 16, v68
	v_and_b32_e32 v135, 0xffff0000, v68
	v_lshlrev_b32_e32 v136, 16, v72
	v_and_b32_e32 v137, 0xffff0000, v72
	v_lshlrev_b32_e32 v138, 16, v76
	v_and_b32_e32 v139, 0xffff0000, v76
	v_lshlrev_b32_e32 v140, 16, v80
	v_and_b32_e32 v141, 0xffff0000, v80
	v_lshlrev_b32_e32 v142, 16, v84
	v_and_b32_e32 v143, 0xffff0000, v84
	v_lshlrev_b32_e32 v144, 16, v88
	v_and_b32_e32 v145, 0xffff0000, v88
	v_add_f32_e32 v194, v124, v126
	v_add_f32_e32 v194, v194, v128
	v_add_f32_e32 v194, v194, v130
	v_add_f32_e32 v194, v194, v132
	v_add_f32_e32 v194, v194, v134
	v_add_f32_e32 v194, v194, v136
	v_add_f32_e32 v194, v194, v138
	v_fma_f32 v194, v194, v226, -v138
	v_add_f32_e32 v195, v125, v127
	v_add_f32_e32 v195, v195, v129
	v_add_f32_e32 v195, v195, v131
	v_add_f32_e32 v195, v195, v133
	v_add_f32_e32 v195, v195, v135
	v_add_f32_e32 v195, v195, v137
	v_add_f32_e32 v195, v195, v139
	v_fma_f32 v195, v195, v226, -v139
	v_add_f32_e32 v202, v126, v128
	v_add_f32_e32 v202, v202, v130
	v_add_f32_e32 v202, v202, v132
	v_add_f32_e32 v202, v202, v134
	v_add_f32_e32 v202, v202, v136
	v_add_f32_e32 v202, v202, v138
	v_add_f32_e32 v202, v202, v140
	v_fma_f32 v202, v202, v227, -v140
	v_add_f32_e32 v203, v127, v129
	v_add_f32_e32 v203, v203, v131
	v_add_f32_e32 v203, v203, v133
	v_add_f32_e32 v203, v203, v135
	v_add_f32_e32 v203, v203, v137
	v_add_f32_e32 v203, v203, v139
	v_add_f32_e32 v203, v203, v141
	v_fma_f32 v203, v203, v227, -v141
	v_add_f32_e32 v210, v128, v130
	v_add_f32_e32 v210, v210, v132
	v_add_f32_e32 v210, v210, v134
	v_add_f32_e32 v210, v210, v136
	v_add_f32_e32 v210, v210, v138
	v_add_f32_e32 v210, v210, v140
	v_add_f32_e32 v210, v210, v142
	v_fma_f32 v210, v210, v228, -v142
	v_add_f32_e32 v211, v129, v131
	v_add_f32_e32 v211, v211, v133
	v_add_f32_e32 v211, v211, v135
	v_add_f32_e32 v211, v211, v137
	v_add_f32_e32 v211, v211, v139
	v_add_f32_e32 v211, v211, v141
	v_add_f32_e32 v211, v211, v143
	v_fma_f32 v211, v211, v228, -v143
	v_add_f32_e32 v218, v130, v132
	v_add_f32_e32 v218, v218, v134
	v_add_f32_e32 v218, v218, v136
	v_add_f32_e32 v218, v218, v138
	v_add_f32_e32 v218, v218, v140
	v_add_f32_e32 v218, v218, v142
	v_add_f32_e32 v218, v218, v144
	v_fma_f32 v218, v218, v229, -v144
	v_add_f32_e32 v219, v131, v133
	v_add_f32_e32 v219, v219, v135
	v_add_f32_e32 v219, v219, v137
	v_add_f32_e32 v219, v219, v139
	v_add_f32_e32 v219, v219, v141
	v_add_f32_e32 v219, v219, v143
	v_add_f32_e32 v219, v219, v145
	v_fma_f32 v219, v219, v229, -v145
	v_lshlrev_b32_e32 v124, 16, v49
	v_and_b32_e32 v125, 0xffff0000, v49
	v_lshlrev_b32_e32 v126, 16, v53
	v_and_b32_e32 v127, 0xffff0000, v53
	v_lshlrev_b32_e32 v128, 16, v57
	v_and_b32_e32 v129, 0xffff0000, v57
	v_lshlrev_b32_e32 v130, 16, v61
	v_and_b32_e32 v131, 0xffff0000, v61
	v_lshlrev_b32_e32 v132, 16, v65
	v_and_b32_e32 v133, 0xffff0000, v65
	v_lshlrev_b32_e32 v134, 16, v69
	v_and_b32_e32 v135, 0xffff0000, v69
	v_lshlrev_b32_e32 v136, 16, v73
	v_and_b32_e32 v137, 0xffff0000, v73
	v_lshlrev_b32_e32 v138, 16, v77
	v_and_b32_e32 v139, 0xffff0000, v77
	v_lshlrev_b32_e32 v140, 16, v81
	v_and_b32_e32 v141, 0xffff0000, v81
	v_lshlrev_b32_e32 v142, 16, v85
	v_and_b32_e32 v143, 0xffff0000, v85
	v_lshlrev_b32_e32 v144, 16, v89
	v_and_b32_e32 v145, 0xffff0000, v89
	v_add_f32_e32 v196, v124, v126
	v_add_f32_e32 v196, v196, v128
	v_add_f32_e32 v196, v196, v130
	v_add_f32_e32 v196, v196, v132
	v_add_f32_e32 v196, v196, v134
	v_add_f32_e32 v196, v196, v136
	v_add_f32_e32 v196, v196, v138
	v_fma_f32 v196, v196, v226, -v138
	v_add_f32_e32 v197, v125, v127
	v_add_f32_e32 v197, v197, v129
	v_add_f32_e32 v197, v197, v131
	v_add_f32_e32 v197, v197, v133
	v_add_f32_e32 v197, v197, v135
	v_add_f32_e32 v197, v197, v137
	v_add_f32_e32 v197, v197, v139
	v_fma_f32 v197, v197, v226, -v139
	v_add_f32_e32 v204, v126, v128
	v_add_f32_e32 v204, v204, v130
	v_add_f32_e32 v204, v204, v132
	v_add_f32_e32 v204, v204, v134
	v_add_f32_e32 v204, v204, v136
	v_add_f32_e32 v204, v204, v138
	v_add_f32_e32 v204, v204, v140
	v_fma_f32 v204, v204, v227, -v140
	v_add_f32_e32 v205, v127, v129
	v_add_f32_e32 v205, v205, v131
	v_add_f32_e32 v205, v205, v133
	v_add_f32_e32 v205, v205, v135
	v_add_f32_e32 v205, v205, v137
	v_add_f32_e32 v205, v205, v139
	v_add_f32_e32 v205, v205, v141
	v_fma_f32 v205, v205, v227, -v141
	v_add_f32_e32 v212, v128, v130
	v_add_f32_e32 v212, v212, v132
	v_add_f32_e32 v212, v212, v134
	v_add_f32_e32 v212, v212, v136
	v_add_f32_e32 v212, v212, v138
	v_add_f32_e32 v212, v212, v140
	v_add_f32_e32 v212, v212, v142
	v_fma_f32 v212, v212, v228, -v142
	v_add_f32_e32 v213, v129, v131
	v_add_f32_e32 v213, v213, v133
	v_add_f32_e32 v213, v213, v135
	v_add_f32_e32 v213, v213, v137
	v_add_f32_e32 v213, v213, v139
	v_add_f32_e32 v213, v213, v141
	v_add_f32_e32 v213, v213, v143
	v_fma_f32 v213, v213, v228, -v143
	v_add_f32_e32 v220, v130, v132
	v_add_f32_e32 v220, v220, v134
	v_add_f32_e32 v220, v220, v136
	v_add_f32_e32 v220, v220, v138
	v_add_f32_e32 v220, v220, v140
	v_add_f32_e32 v220, v220, v142
; __device__ __forceinline__ unsigned pk2(float lo, float hi) { return pg8::cvt_pk_bf16(lo, hi); }
; __device__ __forceinline__ void unpack8(const v4u w, float (&f)[8]) { f[0] = bflo(w.x); f[1] = bfhi(w.x); f[2] = bflo(w.y); f[3] = bfhi(w.y); f[4] = bflo(w.z); f[5] = bfhi(w.z); f[6] = bflo(w.w); f[7] = bfhi(w.w); }
; template <int W> __device__ __forceinline__ void pool_item(Frame& F, int row, int t, int c8) {
;     float s[8], u[8];
; #pragma unroll
;     for (int i = 0; i < 8; ++i) s[i] = 0.f;
;     v4u ld[W];
; #pragma unroll
;     for (int k = 0; k < W; ++k) { const int kk = (t - k) >= 0 ? k : t; ld[k] = *(const v4u*)(F.PROJ + (size_t)(row - kk) * INWP + O_UPOOL + c8); }
; #pragma unroll
;     for (int k = W - 1; k >= 0; --k) { unpack8(ld[k], u); const float wgt = (t - k) >= 0 ? 1.f : 0.f;
; #pragma unroll
;         for (int i = 0; i < 8; ++i) s[i] += wgt * u[i]; }
;     const int cnt = (t + 1) < W ? (t + 1) : W;
;     const float inv = 1.0f / (float)cnt;
;     v4u o; o.x = pk2(s[0] * inv - u[0], s[1] * inv - u[1]); o.y = pk2(s[2] * inv - u[2], s[3] * inv - u[3]); o.z = pk2(s[4] * inv - u[4], s[5] * inv - u[5]); o.w = pk2(s[6] * inv - u[6], s[7] * inv - u[7]);
;     *(v4u*)(F.Y + (size_t)row * 1024 + c8) = o;
; }
	v_add_f32_e32 v220, v220, v144
	v_fma_f32 v220, v220, v229, -v144
	v_add_f32_e32 v221, v131, v133
	v_add_f32_e32 v221, v221, v135
	v_add_f32_e32 v221, v221, v137
	v_add_f32_e32 v221, v221, v139
	v_add_f32_e32 v221, v221, v141
	v_add_f32_e32 v221, v221, v143
	v_add_f32_e32 v221, v221, v145
	v_fma_f32 v221, v221, v229, -v145
	v_lshlrev_b32_e32 v124, 16, v50
	v_and_b32_e32 v125, 0xffff0000, v50
	v_lshlrev_b32_e32 v126, 16, v54
	v_and_b32_e32 v127, 0xffff0000, v54
	v_lshlrev_b32_e32 v128, 16, v58
	v_and_b32_e32 v129, 0xffff0000, v58
	v_lshlrev_b32_e32 v130, 16, v62
	v_and_b32_e32 v131, 0xffff0000, v62
	v_lshlrev_b32_e32 v132, 16, v66
	v_and_b32_e32 v133, 0xffff0000, v66
	v_lshlrev_b32_e32 v134, 16, v70
	v_and_b32_e32 v135, 0xffff0000, v70
	v_lshlrev_b32_e32 v136, 16, v74
	v_and_b32_e32 v137, 0xffff0000, v74
	v_lshlrev_b32_e32 v138, 16, v78
	v_and_b32_e32 v139, 0xffff0000, v78
	v_lshlrev_b32_e32 v140, 16, v82
	v_and_b32_e32 v141, 0xffff0000, v82
	v_lshlrev_b32_e32 v142, 16, v86
	v_and_b32_e32 v143, 0xffff0000, v86
	v_lshlrev_b32_e32 v144, 16, v90
	v_and_b32_e32 v145, 0xffff0000, v90
	v_add_f32_e32 v198, v124, v126
	v_add_f32_e32 v198, v198, v128
	v_add_f32_e32 v198, v198, v130
	v_add_f32_e32 v198, v198, v132
	v_add_f32_e32 v198, v198, v134
	v_add_f32_e32 v198, v198, v136
	v_add_f32_e32 v198, v198, v138
	v_fma_f32 v198, v198, v226, -v138
	v_add_f32_e32 v199, v125, v127
	v_add_f32_e32 v199, v199, v129
	v_add_f32_e32 v199, v199, v131
	v_add_f32_e32 v199, v199, v133
	v_add_f32_e32 v199, v199, v135
	v_add_f32_e32 v199, v199, v137
	v_add_f32_e32 v199, v199, v139
	v_fma_f32 v199, v199, v226, -v139
	v_add_f32_e32 v206, v126, v128
	v_add_f32_e32 v206, v206, v130
	v_add_f32_e32 v206, v206, v132
	v_add_f32_e32 v206, v206, v134
	v_add_f32_e32 v206, v206, v136
	v_add_f32_e32 v206, v206, v138
	v_add_f32_e32 v206, v206, v140
	v_fma_f32 v206, v206, v227, -v140
	v_add_f32_e32 v207, v127, v129
	v_add_f32_e32 v207, v207, v131
	v_add_f32_e32 v207, v207, v133
	v_add_f32_e32 v207, v207, v135
	v_add_f32_e32 v207, v207, v137
	v_add_f32_e32 v207, v207, v139
	v_add_f32_e32 v207, v207, v141
	v_fma_f32 v207, v207, v227, -v141
	v_add_f32_e32 v214, v128, v130
	v_add_f32_e32 v214, v214, v132
	v_add_f32_e32 v214, v214, v134
	v_add_f32_e32 v214, v214, v136
	v_add_f32_e32 v214, v214, v138
	v_add_f32_e32 v214, v214, v140
	v_add_f32_e32 v214, v214, v142
	v_fma_f32 v214, v214, v228, -v142
	v_add_f32_e32 v215, v129, v131
	v_add_f32_e32 v215, v215, v133
	v_add_f32_e32 v215, v215, v135
	v_add_f32_e32 v215, v215, v137
	v_add_f32_e32 v215, v215, v139
	v_add_f32_e32 v215, v215, v141
	v_add_f32_e32 v215, v215, v143
	v_fma_f32 v215, v215, v228, -v143
	v_add_f32_e32 v222, v130, v132
	v_add_f32_e32 v222, v222, v134
	v_add_f32_e32 v222, v222, v136
	v_add_f32_e32 v222, v222, v138
	v_add_f32_e32 v222, v222, v140
	v_add_f32_e32 v222, v222, v142
	v_add_f32_e32 v222, v222, v144
	v_fma_f32 v222, v222, v229, -v144
	v_add_f32_e32 v223, v131, v133
	v_add_f32_e32 v223, v223, v135
	v_add_f32_e32 v223, v223, v137
	v_add_f32_e32 v223, v223, v139
	v_add_f32_e32 v223, v223, v141
	v_add_f32_e32 v223, v223, v143
	v_add_f32_e32 v223, v223, v145
	v_fma_f32 v223, v223, v229, -v145
	v_lshlrev_b32_e32 v124, 16, v51
	v_and_b32_e32 v125, 0xffff0000, v51
	v_lshlrev_b32_e32 v126, 16, v55
	v_and_b32_e32 v127, 0xffff0000, v55
	v_lshlrev_b32_e32 v128, 16, v59
	v_and_b32_e32 v129, 0xffff0000, v59
	v_lshlrev_b32_e32 v130, 16, v63
	v_and_b32_e32 v131, 0xffff0000, v63
	v_lshlrev_b32_e32 v132, 16, v67
	v_and_b32_e32 v133, 0xffff0000, v67
	v_lshlrev_b32_e32 v134, 16, v71
	v_and_b32_e32 v135, 0xffff0000, v71
	v_lshlrev_b32_e32 v136, 16, v75
	v_and_b32_e32 v137, 0xffff0000, v75
	v_lshlrev_b32_e32 v138, 16, v79
	v_and_b32_e32 v139, 0xffff0000, v79
	v_lshlrev_b32_e32 v140, 16, v83
	v_and_b32_e32 v141, 0xffff0000, v83
	v_lshlrev_b32_e32 v142, 16, v87
	v_and_b32_e32 v143, 0xffff0000, v87
	v_lshlrev_b32_e32 v144, 16, v91
	v_and_b32_e32 v145, 0xffff0000, v91
	v_add_f32_e32 v200, v124, v126
	v_add_f32_e32 v200, v200, v128
	v_add_f32_e32 v200, v200, v130
	v_add_f32_e32 v200, v200, v132
	v_add_f32_e32 v200, v200, v134
	v_add_f32_e32 v200, v200, v136
	v_add_f32_e32 v200, v200, v138
	v_fma_f32 v200, v200, v226, -v138
	v_add_f32_e32 v201, v125, v127
	v_add_f32_e32 v201, v201, v129
	v_add_f32_e32 v201, v201, v131
	v_add_f32_e32 v201, v201, v133
	v_add_f32_e32 v201, v201, v135
	v_add_f32_e32 v201, v201, v137
	v_add_f32_e32 v201, v201, v139
	v_fma_f32 v201, v201, v226, -v139
	v_add_f32_e32 v208, v126, v128
	v_add_f32_e32 v208, v208, v130
	v_add_f32_e32 v208, v208, v132
	v_add_f32_e32 v208, v208, v134
	v_add_f32_e32 v208, v208, v136
	v_add_f32_e32 v208, v208, v138
	v_add_f32_e32 v208, v208, v140
	v_fma_f32 v208, v208, v227, -v140
	v_add_f32_e32 v209, v127, v129
	v_add_f32_e32 v209, v209, v131
	v_add_f32_e32 v209, v209, v133
	v_add_f32_e32 v209, v209, v135
	v_add_f32_e32 v209, v209, v137
	v_add_f32_e32 v209, v209, v139
	v_add_f32_e32 v209, v209, v141
	v_fma_f32 v209, v209, v227, -v141
	v_add_f32_e32 v216, v128, v130
	v_add_f32_e32 v216, v216, v132
	v_add_f32_e32 v216, v216, v134
	v_add_f32_e32 v216, v216, v136
	v_add_f32_e32 v216, v216, v138
	v_add_f32_e32 v216, v216, v140
	v_add_f32_e32 v216, v216, v142
	v_fma_f32 v216, v216, v228, -v142
	v_add_f32_e32 v217, v129, v131
	v_add_f32_e32 v217, v217, v133
	v_add_f32_e32 v217, v217, v135
	v_add_f32_e32 v217, v217, v137
	v_add_f32_e32 v217, v217, v139
	v_add_f32_e32 v217, v217, v141
	v_add_f32_e32 v217, v217, v143
	v_fma_f32 v217, v217, v228, -v143
	v_add_f32_e32 v224, v130, v132
	v_add_f32_e32 v224, v224, v134
	v_add_f32_e32 v224, v224, v136
	v_add_f32_e32 v224, v224, v138
	v_add_f32_e32 v224, v224, v140
	v_add_f32_e32 v224, v224, v142
	v_add_f32_e32 v224, v224, v144
	v_fma_f32 v224, v224, v229, -v144
	v_add_f32_e32 v225, v131, v133
	v_add_f32_e32 v225, v225, v135
	v_add_f32_e32 v225, v225, v137
	v_add_f32_e32 v225, v225, v139
	v_add_f32_e32 v225, v225, v141
	v_add_f32_e32 v225, v225, v143
	v_add_f32_e32 v225, v225, v145
	v_fma_f32 v225, v225, v229, -v145
	v_cvt_pk_bf16_f32 v194, v194, v195
	v_cvt_pk_bf16_f32 v195, v196, v197
	v_cvt_pk_bf16_f32 v196, v198, v199
	v_cvt_pk_bf16_f32 v197, v200, v201
	global_store_dwordx4 v17, v[194:197], s[14:15] nt
	v_cvt_pk_bf16_f32 v202, v202, v203
	v_cvt_pk_bf16_f32 v203, v204, v205
	v_cvt_pk_bf16_f32 v204, v206, v207
	v_cvt_pk_bf16_f32 v205, v208, v209
	v_add_u32_e32 v13, 0x800, v17
	global_store_dwordx4 v13, v[202:205], s[14:15] nt
	v_cvt_pk_bf16_f32 v210, v210, v211
	v_cvt_pk_bf16_f32 v211, v212, v213
	v_cvt_pk_bf16_f32 v212, v214, v215
	v_cvt_pk_bf16_f32 v213, v216, v217
	v_add_u32_e32 v13, 0x1000, v17
	global_store_dwordx4 v13, v[210:213], s[14:15] nt
	v_cvt_pk_bf16_f32 v218, v218, v219
	v_cvt_pk_bf16_f32 v219, v220, v221
	v_cvt_pk_bf16_f32 v220, v222, v223
	v_cvt_pk_bf16_f32 v221, v224, v225
	v_add_u32_e32 v13, 0x1800, v17
	global_store_dwordx4 v13, v[218:221], s[14:15] nt
; __device__ __forceinline__ unsigned pk2(float lo, float hi) { return pg8::cvt_pk_bf16(lo, hi); }
; __device__ __forceinline__ void unpack8(const v4u w, float (&f)[8]) { f[0] = bflo(w.x); f[1] = bfhi(w.x); f[2] = bflo(w.y); f[3] = bfhi(w.y); f[4] = bflo(w.z); f[5] = bfhi(w.z); f[6] = bflo(w.w); f[7] = bfhi(w.w); }
; __device__ __forceinline__ void poolconv_phase(Frame& F, const float* conv_w_l) {
;     ...
;     for (int idx = gt; idx < M * 128; idx += NGT) {
;         const int row = idx >> 7, c8 = (idx & 127) * 8, t = row & (SEQ - 1);
;         float acc[8], a[8], b[8];
; #pragma unroll
;         for (int i = 0; i < 8; ++i) acc[i] = 0.f;
;         v4u la[3], lb[3];
; #pragma unroll
;         for (int j = 0; j < 3; ++j) { const int back = (t - 2 + j) >= 0 ? (2 - j) : 0; const bf16* pr = F.PROJ + (size_t)(row - back) * INWP; la[j] = *(const v4u*)(pr + O_CG + c8); lb[j] = *(const v4u*)(pr + O_UCONV + c8); }
;         const v4u lg = *(const v4u*)(F.PROJ + (size_t)row * INWP + O_BG + c8);
; #pragma unroll
;         for (int j = 0; j < 3; ++j) { const float wgt = (t - 2 + j) >= 0 ? 1.f : 0.f; unpack8(la[j], a); unpack8(lb[j], b);
;             const f32x4 w0 = *(const f32x4*)(conv_w_l + j * 1024 + c8) * wgt, w1 = *(const f32x4*)(conv_w_l + j * 1024 + c8 + 4) * wgt;
;             acc[0] += w0.x * (a[0] * b[0]); acc[1] += w0.y * (a[1] * b[1]); acc[2] += w0.z * (a[2] * b[2]); acc[3] += w0.w * (a[3] * b[3]);
;             acc[4] += w1.x * (a[4] * b[4]); acc[5] += w1.y * (a[5] * b[5]); acc[6] += w1.z * (a[6] * b[6]); acc[7] += w1.w * (a[7] * b[7]); }
;         unpack8(lg, a);
;         v4u o; o.x = pk2(a[0] * acc[0], a[1] * acc[1]); o.y = pk2(a[2] * acc[2], a[3] * acc[3]); o.z = pk2(a[4] * acc[4], a[5] * acc[5]); o.w = pk2(a[6] * acc[6], a[7] * acc[7]);
;         *(v4u*)(F.Y + (size_t)M * 1024 + (size_t)row * 1024 + c8) = o;
.Lpc_conv:
	s_mul_i32 s10, s10, 0x3000
	s_add_u32 s12, s86, s10
	s_addc_u32 s13, s87, 0
	v_and_b32_e32 v3, 0x7f, v1
	v_lshrrev_b32_e32 v2, 7, v1
	v_lshlrev_b32_e32 v8, 5, v3
	global_load_dwordx4 v[148:151], v8, s[12:13] offset:0
	global_load_dwordx4 v[152:155], v8, s[12:13] offset:16
	v_add_u32_e32 v8, 0x1000, v8
	global_load_dwordx4 v[156:159], v8, s[12:13] offset:0
	global_load_dwordx4 v[160:163], v8, s[12:13] offset:16
	v_add_u32_e32 v8, 0x1000, v8
	global_load_dwordx4 v[164:167], v8, s[12:13] offset:0
	global_load_dwordx4 v[168:171], v8, s[12:13] offset:16
	v_lshlrev_b32_e32 v8, 4, v3
	v_add_u32_e32 v19, 0x800, v8
	s_add_u32 s14, s14, 0x1000000
	s_addc_u32 s15, s15, 0
	v_lshlrev_b32_e32 v4, 2, v2
	v_and_b32_e32 v5, 0x7ff, v4
	v_mul_u32_u24_e32 v6, 0x3600, v5
	v_mul_u32_u24_e32 v7, 0x3600, v4
	v_add_u32_e32 v7, v7, v19
	v_lshl_add_u32 v16, v4, 11, v8
	v_min_u32_e32 v11, 0x6c00, v6
	v_sub_u32_e32 v12, v7, v11
	global_load_dwordx4 v[20:23], v12, s[96:97] offset:2048 nt
	global_load_dwordx4 v[44:47], v12, s[96:97] nt
	v_min_u32_e32 v11, 0x3600, v6
	v_sub_u32_e32 v12, v7, v11
	global_load_dwordx4 v[24:27], v12, s[96:97] offset:2048 nt
	global_load_dwordx4 v[48:51], v12, s[96:97] nt
	v_mov_b32_e32 v12, v7
	global_load_dwordx4 v[28:31], v12, s[96:97] offset:2048 nt
	global_load_dwordx4 v[52:55], v12, s[96:97] nt
	v_add_u32_e32 v13, 0x1000, v12
	global_load_dwordx4 v[68:71], v13, s[96:97] nt
	v_add_u32_e32 v12, 0x3600, v7
	global_load_dwordx4 v[32:35], v12, s[96:97] offset:2048 nt
	global_load_dwordx4 v[56:59], v12, s[96:97] nt
	v_add_u32_e32 v13, 0x1000, v12
	global_load_dwordx4 v[72:75], v13, s[96:97] nt
	v_add_u32_e32 v12, 0x6c00, v7
	global_load_dwordx4 v[36:39], v12, s[96:97] offset:2048 nt
	global_load_dwordx4 v[60:63], v12, s[96:97] nt
	v_add_u32_e32 v13, 0x1000, v12
	global_load_dwordx4 v[76:79], v13, s[96:97] nt
	v_add_u32_e32 v12, 0xa200, v7
	global_load_dwordx4 v[40:43], v12, s[96:97] offset:2048 nt
	global_load_dwordx4 v[64:67], v12, s[96:97] nt
	v_add_u32_e32 v13, 0x1000, v12
	global_load_dwordx4 v[80:83], v13, s[96:97] nt
	v_lshlrev_b32_e32 v4, 2, v2
	v_add_u32_e32 v4, 0x1000, v4
	v_and_b32_e32 v18, 0x7ff, v4
	v_mul_u32_u24_e32 v6, 0x3600, v18
	v_mul_u32_u24_e32 v7, 0x3600, v4
	v_add_u32_e32 v7, v7, v19
	v_lshl_add_u32 v17, v4, 11, v8
	v_min_u32_e32 v11, 0x6c00, v6
	v_sub_u32_e32 v12, v7, v11
	global_load_dwordx4 v[84:87], v12, s[96:97] offset:2048 nt
	global_load_dwordx4 v[108:111], v12, s[96:97] nt
	v_min_u32_e32 v11, 0x3600, v6
	v_sub_u32_e32 v12, v7, v11
	global_load_dwordx4 v[88:91], v12, s[96:97] offset:2048 nt
	global_load_dwordx4 v[112:115], v12, s[96:97] nt
	v_mov_b32_e32 v12, v7
	global_load_dwordx4 v[92:95], v12, s[96:97] offset:2048 nt
	global_load_dwordx4 v[116:119], v12, s[96:97] nt
	v_add_u32_e32 v13, 0x1000, v12
	global_load_dwordx4 v[132:135], v13, s[96:97] nt
	v_add_u32_e32 v12, 0x3600, v7
	global_load_dwordx4 v[96:99], v12, s[96:97] offset:2048 nt
	global_load_dwordx4 v[120:123], v12, s[96:97] nt
	v_add_u32_e32 v13, 0x1000, v12
	global_load_dwordx4 v[136:139], v13, s[96:97] nt
	v_add_u32_e32 v12, 0x6c00, v7
	global_load_dwordx4 v[100:103], v12, s[96:97] offset:2048 nt
	global_load_dwordx4 v[124:127], v12, s[96:97] nt
	v_add_u32_e32 v13, 0x1000, v12
	global_load_dwordx4 v[140:143], v13, s[96:97] nt
	v_add_u32_e32 v12, 0xa200, v7
	global_load_dwordx4 v[104:107], v12, s[96:97] offset:2048 nt
	global_load_dwordx4 v[128:131], v12, s[96:97] nt
	v_add_u32_e32 v13, 0x1000, v12
	global_load_dwordx4 v[144:147], v13, s[96:97] nt
	s_waitcnt vmcnt(16)
	v_cmp_le_u32_e32 vcc, 2, v5
	s_nop 1
	v_cndmask_b32_e32 v20, 0, v20, vcc
	v_cndmask_b32_e32 v21, 0, v21, vcc
	v_cndmask_b32_e32 v22, 0, v22, vcc
	v_cndmask_b32_e32 v23, 0, v23, vcc
	v_cmp_le_u32_e32 vcc, 1, v5
	s_nop 1
	v_cndmask_b32_e32 v24, 0, v24, vcc
	v_cndmask_b32_e32 v25, 0, v25, vcc
	v_cndmask_b32_e32 v26, 0, v26, vcc
	v_cndmask_b32_e32 v27, 0, v27, vcc
	v_lshlrev_b32_e32 v172, 16, v20
	v_and_b32_e32 v173, 0xffff0000, v20
	v_lshlrev_b32_e32 v174, 16, v44
	v_and_b32_e32 v175, 0xffff0000, v44
	v_mul_f32_e32 v194, v172, v174
	v_mul_f32_e32 v195, v173, v175
	v_lshlrev_b32_e32 v172, 16, v21
	v_and_b32_e32 v173, 0xffff0000, v21
	v_lshlrev_b32_e32 v174, 16, v45
	v_and_b32_e32 v175, 0xffff0000, v45
	v_mul_f32_e32 v196, v172, v174
	v_mul_f32_e32 v197, v173, v175
	v_lshlrev_b32_e32 v172, 16, v22
	v_and_b32_e32 v173, 0xffff0000, v22
	v_lshlrev_b32_e32 v174, 16, v46
	v_and_b32_e32 v175, 0xffff0000, v46
	v_mul_f32_e32 v198, v172, v174
	v_mul_f32_e32 v199, v173, v175
	v_lshlrev_b32_e32 v172, 16, v23
	v_and_b32_e32 v173, 0xffff0000, v23
	v_lshlrev_b32_e32 v174, 16, v47
	v_and_b32_e32 v175, 0xffff0000, v47
	v_mul_f32_e32 v200, v172, v174
	v_mul_f32_e32 v201, v173, v175
	v_lshlrev_b32_e32 v172, 16, v24
	v_and_b32_e32 v173, 0xffff0000, v24
	v_lshlrev_b32_e32 v174, 16, v48
	v_and_b32_e32 v175, 0xffff0000, v48
	v_mul_f32_e32 v202, v172, v174
	v_mul_f32_e32 v203, v173, v175
	v_lshlrev_b32_e32 v172, 16, v25
	v_and_b32_e32 v173, 0xffff0000, v25
	v_lshlrev_b32_e32 v174, 16, v49
	v_and_b32_e32 v175, 0xffff0000, v49
	v_mul_f32_e32 v204, v172, v174
	v_mul_f32_e32 v205, v173, v175
	v_lshlrev_b32_e32 v172, 16, v26
	v_and_b32_e32 v173, 0xffff0000, v26
	v_lshlrev_b32_e32 v174, 16, v50
	v_and_b32_e32 v175, 0xffff0000, v50
	v_mul_f32_e32 v206, v172, v174
	v_mul_f32_e32 v207, v173, v175
	v_lshlrev_b32_e32 v172, 16, v27
	v_and_b32_e32 v173, 0xffff0000, v27
	v_lshlrev_b32_e32 v174, 16, v51
	v_and_b32_e32 v175, 0xffff0000, v51
	v_mul_f32_e32 v208, v172, v174
	v_mul_f32_e32 v209, v173, v175
	v_lshlrev_b32_e32 v172, 16, v28
	v_and_b32_e32 v173, 0xffff0000, v28
	v_lshlrev_b32_e32 v174, 16, v52
; __device__ __forceinline__ unsigned pk2(float lo, float hi) { return pg8::cvt_pk_bf16(lo, hi); }
; __device__ __forceinline__ void unpack8(const v4u w, float (&f)[8]) { f[0] = bflo(w.x); f[1] = bfhi(w.x); f[2] = bflo(w.y); f[3] = bfhi(w.y); f[4] = bflo(w.z); f[5] = bfhi(w.z); f[6] = bflo(w.w); f[7] = bfhi(w.w); }
; __device__ __forceinline__ void poolconv_phase(Frame& F, const float* conv_w_l) {
;     ...
;     for (int idx = gt; idx < M * 128; idx += NGT) {
;         const int row = idx >> 7, c8 = (idx & 127) * 8, t = row & (SEQ - 1);
;         float acc[8], a[8], b[8];
; #pragma unroll
;         for (int i = 0; i < 8; ++i) acc[i] = 0.f;
;         v4u la[3], lb[3];
; #pragma unroll
;         for (int j = 0; j < 3; ++j) { const int back = (t - 2 + j) >= 0 ? (2 - j) : 0; const bf16* pr = F.PROJ + (size_t)(row - back) * INWP; la[j] = *(const v4u*)(pr + O_CG + c8); lb[j] = *(const v4u*)(pr + O_UCONV + c8); }
;         const v4u lg = *(const v4u*)(F.PROJ + (size_t)row * INWP + O_BG + c8);
; #pragma unroll
;         for (int j = 0; j < 3; ++j) { const float wgt = (t - 2 + j) >= 0 ? 1.f : 0.f; unpack8(la[j], a); unpack8(lb[j], b);
;             const f32x4 w0 = *(const f32x4*)(conv_w_l + j * 1024 + c8) * wgt, w1 = *(const f32x4*)(conv_w_l + j * 1024 + c8 + 4) * wgt;
;             acc[0] += w0.x * (a[0] * b[0]); acc[1] += w0.y * (a[1] * b[1]); acc[2] += w0.z * (a[2] * b[2]); acc[3] += w0.w * (a[3] * b[3]);
;             acc[4] += w1.x * (a[4] * b[4]); acc[5] += w1.y * (a[5] * b[5]); acc[6] += w1.z * (a[6] * b[6]); acc[7] += w1.w * (a[7] * b[7]); }
;         unpack8(lg, a);
;         v4u o; o.x = pk2(a[0] * acc[0], a[1] * acc[1]); o.y = pk2(a[2] * acc[2], a[3] * acc[3]); o.z = pk2(a[4] * acc[4], a[5] * acc[5]); o.w = pk2(a[6] * acc[6], a[7] * acc[7]);
;         *(v4u*)(F.Y + (size_t)M * 1024 + (size_t)row * 1024 + c8) = o;
	v_and_b32_e32 v175, 0xffff0000, v52
	v_mul_f32_e32 v210, v172, v174
	v_mul_f32_e32 v211, v173, v175
	v_lshlrev_b32_e32 v172, 16, v29
	v_and_b32_e32 v173, 0xffff0000, v29
	v_lshlrev_b32_e32 v174, 16, v53
	v_and_b32_e32 v175, 0xffff0000, v53
	v_mul_f32_e32 v212, v172, v174
	v_mul_f32_e32 v213, v173, v175
	v_lshlrev_b32_e32 v172, 16, v30
	v_and_b32_e32 v173, 0xffff0000, v30
	v_lshlrev_b32_e32 v174, 16, v54
	v_and_b32_e32 v175, 0xffff0000, v54
	v_mul_f32_e32 v214, v172, v174
	v_mul_f32_e32 v215, v173, v175
	v_lshlrev_b32_e32 v172, 16, v31
	v_and_b32_e32 v173, 0xffff0000, v31
	v_lshlrev_b32_e32 v174, 16, v55
	v_and_b32_e32 v175, 0xffff0000, v55
	v_mul_f32_e32 v216, v172, v174
	v_mul_f32_e32 v217, v173, v175
	v_lshlrev_b32_e32 v172, 16, v32
	v_and_b32_e32 v173, 0xffff0000, v32
	v_lshlrev_b32_e32 v174, 16, v56
	v_and_b32_e32 v175, 0xffff0000, v56
	v_mul_f32_e32 v218, v172, v174
	v_mul_f32_e32 v219, v173, v175
	v_lshlrev_b32_e32 v172, 16, v33
	v_and_b32_e32 v173, 0xffff0000, v33
	v_lshlrev_b32_e32 v174, 16, v57
	v_and_b32_e32 v175, 0xffff0000, v57
	v_mul_f32_e32 v220, v172, v174
	v_mul_f32_e32 v221, v173, v175
	v_lshlrev_b32_e32 v172, 16, v34
	v_and_b32_e32 v173, 0xffff0000, v34
	v_lshlrev_b32_e32 v174, 16, v58
	v_and_b32_e32 v175, 0xffff0000, v58
	v_mul_f32_e32 v222, v172, v174
	v_mul_f32_e32 v223, v173, v175
	v_lshlrev_b32_e32 v172, 16, v35
	v_and_b32_e32 v173, 0xffff0000, v35
	v_lshlrev_b32_e32 v174, 16, v59
	v_and_b32_e32 v175, 0xffff0000, v59
	v_mul_f32_e32 v224, v172, v174
	v_mul_f32_e32 v225, v173, v175
	v_lshlrev_b32_e32 v172, 16, v36
	v_and_b32_e32 v173, 0xffff0000, v36
	v_lshlrev_b32_e32 v174, 16, v60
	v_and_b32_e32 v175, 0xffff0000, v60
	v_mul_f32_e32 v226, v172, v174
	v_mul_f32_e32 v227, v173, v175
	v_lshlrev_b32_e32 v172, 16, v37
	v_and_b32_e32 v173, 0xffff0000, v37
	v_lshlrev_b32_e32 v174, 16, v61
	v_and_b32_e32 v175, 0xffff0000, v61
	v_mul_f32_e32 v228, v172, v174
	v_mul_f32_e32 v229, v173, v175
	v_lshlrev_b32_e32 v172, 16, v38
	v_and_b32_e32 v173, 0xffff0000, v38
	v_lshlrev_b32_e32 v174, 16, v62
	v_and_b32_e32 v175, 0xffff0000, v62
	v_mul_f32_e32 v230, v172, v174
	v_mul_f32_e32 v231, v173, v175
	v_lshlrev_b32_e32 v172, 16, v39
	v_and_b32_e32 v173, 0xffff0000, v39
	v_lshlrev_b32_e32 v174, 16, v63
	v_and_b32_e32 v175, 0xffff0000, v63
	v_mul_f32_e32 v232, v172, v174
	v_mul_f32_e32 v233, v173, v175
	v_lshlrev_b32_e32 v172, 16, v40
	v_and_b32_e32 v173, 0xffff0000, v40
	v_lshlrev_b32_e32 v174, 16, v64
	v_and_b32_e32 v175, 0xffff0000, v64
	v_mul_f32_e32 v234, v172, v174
	v_mul_f32_e32 v235, v173, v175
	v_lshlrev_b32_e32 v172, 16, v41
	v_and_b32_e32 v173, 0xffff0000, v41
	v_lshlrev_b32_e32 v174, 16, v65
	v_and_b32_e32 v175, 0xffff0000, v65
	v_mul_f32_e32 v236, v172, v174
	v_mul_f32_e32 v237, v173, v175
	v_lshlrev_b32_e32 v172, 16, v42
	v_and_b32_e32 v173, 0xffff0000, v42
	v_lshlrev_b32_e32 v174, 16, v66
	v_and_b32_e32 v175, 0xffff0000, v66
	v_mul_f32_e32 v238, v172, v174
	v_mul_f32_e32 v239, v173, v175
	v_lshlrev_b32_e32 v172, 16, v43
	v_and_b32_e32 v173, 0xffff0000, v43
	v_lshlrev_b32_e32 v174, 16, v67
	v_and_b32_e32 v175, 0xffff0000, v67
	v_mul_f32_e32 v240, v172, v174
	v_mul_f32_e32 v241, v173, v175
	v_lshlrev_b32_e32 v172, 16, v68
	v_and_b32_e32 v173, 0xffff0000, v68
	v_mul_f32_e32 v176, v148, v194
	v_fmac_f32_e32 v176, v156, v202
	v_fmac_f32_e32 v176, v164, v210
	v_mul_f32_e32 v176, v172, v176
	v_mul_f32_e32 v177, v149, v195
	v_fmac_f32_e32 v177, v157, v203
	v_fmac_f32_e32 v177, v165, v211
	v_mul_f32_e32 v177, v173, v177
	v_lshlrev_b32_e32 v172, 16, v69
	v_and_b32_e32 v173, 0xffff0000, v69
	v_mul_f32_e32 v178, v150, v196
	v_fmac_f32_e32 v178, v158, v204
	v_fmac_f32_e32 v178, v166, v212
	v_mul_f32_e32 v178, v172, v178
	v_mul_f32_e32 v179, v151, v197
	v_fmac_f32_e32 v179, v159, v205
	v_fmac_f32_e32 v179, v167, v213
	v_mul_f32_e32 v179, v173, v179
	v_lshlrev_b32_e32 v172, 16, v70
	v_and_b32_e32 v173, 0xffff0000, v70
	v_mul_f32_e32 v180, v152, v198
	v_fmac_f32_e32 v180, v160, v206
	v_fmac_f32_e32 v180, v168, v214
	v_mul_f32_e32 v180, v172, v180
	v_mul_f32_e32 v181, v153, v199
	v_fmac_f32_e32 v181, v161, v207
	v_fmac_f32_e32 v181, v169, v215
	v_mul_f32_e32 v181, v173, v181
	v_lshlrev_b32_e32 v172, 16, v71
	v_and_b32_e32 v173, 0xffff0000, v71
	v_mul_f32_e32 v182, v154, v200
	v_fmac_f32_e32 v182, v162, v208
	v_fmac_f32_e32 v182, v170, v216
	v_mul_f32_e32 v182, v172, v182
	v_mul_f32_e32 v183, v155, v201
	v_fmac_f32_e32 v183, v163, v209
	v_fmac_f32_e32 v183, v171, v217
	v_mul_f32_e32 v183, v173, v183
	v_cvt_pk_bf16_f32 v184, v176, v177
	v_cvt_pk_bf16_f32 v185, v178, v179
	v_cvt_pk_bf16_f32 v186, v180, v181
	v_cvt_pk_bf16_f32 v187, v182, v183
	global_store_dwordx4 v16, v[184:187], s[14:15] nt
	s_nop 1
	v_lshlrev_b32_e32 v172, 16, v72
	v_and_b32_e32 v173, 0xffff0000, v72
	v_mul_f32_e32 v176, v148, v202
	v_fmac_f32_e32 v176, v156, v210
	v_fmac_f32_e32 v176, v164, v218
	v_mul_f32_e32 v176, v172, v176
	v_mul_f32_e32 v177, v149, v203
	v_fmac_f32_e32 v177, v157, v211
	v_fmac_f32_e32 v177, v165, v219
	v_mul_f32_e32 v177, v173, v177
	v_lshlrev_b32_e32 v172, 16, v73
	v_and_b32_e32 v173, 0xffff0000, v73
	v_mul_f32_e32 v178, v150, v204
	v_fmac_f32_e32 v178, v158, v212
	v_fmac_f32_e32 v178, v166, v220
	v_mul_f32_e32 v178, v172, v178
	v_mul_f32_e32 v179, v151, v205
	v_fmac_f32_e32 v179, v159, v213
	v_fmac_f32_e32 v179, v167, v221
	v_mul_f32_e32 v179, v173, v179
	v_lshlrev_b32_e32 v172, 16, v74
	v_and_b32_e32 v173, 0xffff0000, v74
	v_mul_f32_e32 v180, v152, v206
	v_fmac_f32_e32 v180, v160, v214
	v_fmac_f32_e32 v180, v168, v222
	v_mul_f32_e32 v180, v172, v180
	v_mul_f32_e32 v181, v153, v207
	v_fmac_f32_e32 v181, v161, v215
	v_fmac_f32_e32 v181, v169, v223
; __device__ __forceinline__ unsigned pk2(float lo, float hi) { return pg8::cvt_pk_bf16(lo, hi); }
; __device__ __forceinline__ void unpack8(const v4u w, float (&f)[8]) { f[0] = bflo(w.x); f[1] = bfhi(w.x); f[2] = bflo(w.y); f[3] = bfhi(w.y); f[4] = bflo(w.z); f[5] = bfhi(w.z); f[6] = bflo(w.w); f[7] = bfhi(w.w); }
; __device__ __forceinline__ void poolconv_phase(Frame& F, const float* conv_w_l) {
;     ...
;     for (int idx = gt; idx < M * 128; idx += NGT) {
;         const int row = idx >> 7, c8 = (idx & 127) * 8, t = row & (SEQ - 1);
;         float acc[8], a[8], b[8];
; #pragma unroll
;         for (int i = 0; i < 8; ++i) acc[i] = 0.f;
;         v4u la[3], lb[3];
; #pragma unroll
;         for (int j = 0; j < 3; ++j) { const int back = (t - 2 + j) >= 0 ? (2 - j) : 0; const bf16* pr = F.PROJ + (size_t)(row - back) * INWP; la[j] = *(const v4u*)(pr + O_CG + c8); lb[j] = *(const v4u*)(pr + O_UCONV + c8); }
;         const v4u lg = *(const v4u*)(F.PROJ + (size_t)row * INWP + O_BG + c8);
; #pragma unroll
;         for (int j = 0; j < 3; ++j) { const float wgt = (t - 2 + j) >= 0 ? 1.f : 0.f; unpack8(la[j], a); unpack8(lb[j], b);
;             const f32x4 w0 = *(const f32x4*)(conv_w_l + j * 1024 + c8) * wgt, w1 = *(const f32x4*)(conv_w_l + j * 1024 + c8 + 4) * wgt;
;             acc[0] += w0.x * (a[0] * b[0]); acc[1] += w0.y * (a[1] * b[1]); acc[2] += w0.z * (a[2] * b[2]); acc[3] += w0.w * (a[3] * b[3]);
;             acc[4] += w1.x * (a[4] * b[4]); acc[5] += w1.y * (a[5] * b[5]); acc[6] += w1.z * (a[6] * b[6]); acc[7] += w1.w * (a[7] * b[7]); }
;         unpack8(lg, a);
;         v4u o; o.x = pk2(a[0] * acc[0], a[1] * acc[1]); o.y = pk2(a[2] * acc[2], a[3] * acc[3]); o.z = pk2(a[4] * acc[4], a[5] * acc[5]); o.w = pk2(a[6] * acc[6], a[7] * acc[7]);
;         *(v4u*)(F.Y + (size_t)M * 1024 + (size_t)row * 1024 + c8) = o;
	v_mul_f32_e32 v181, v173, v181
	v_lshlrev_b32_e32 v172, 16, v75
	v_and_b32_e32 v173, 0xffff0000, v75
	v_mul_f32_e32 v182, v154, v208
	v_fmac_f32_e32 v182, v162, v216
	v_fmac_f32_e32 v182, v170, v224
	v_mul_f32_e32 v182, v172, v182
	v_mul_f32_e32 v183, v155, v209
	v_fmac_f32_e32 v183, v163, v217
	v_fmac_f32_e32 v183, v171, v225
	v_mul_f32_e32 v183, v173, v183
	v_cvt_pk_bf16_f32 v184, v176, v177
	v_cvt_pk_bf16_f32 v185, v178, v179
	v_cvt_pk_bf16_f32 v186, v180, v181
	v_cvt_pk_bf16_f32 v187, v182, v183
	v_add_u32_e32 v13, 0x800, v16
	global_store_dwordx4 v13, v[184:187], s[14:15] nt
	s_nop 1
	v_lshlrev_b32_e32 v172, 16, v76
	v_and_b32_e32 v173, 0xffff0000, v76
	v_mul_f32_e32 v176, v148, v210
	v_fmac_f32_e32 v176, v156, v218
	v_fmac_f32_e32 v176, v164, v226
	v_mul_f32_e32 v176, v172, v176
	v_mul_f32_e32 v177, v149, v211
	v_fmac_f32_e32 v177, v157, v219
	v_fmac_f32_e32 v177, v165, v227
	v_mul_f32_e32 v177, v173, v177
	v_lshlrev_b32_e32 v172, 16, v77
	v_and_b32_e32 v173, 0xffff0000, v77
	v_mul_f32_e32 v178, v150, v212
	v_fmac_f32_e32 v178, v158, v220
	v_fmac_f32_e32 v178, v166, v228
	v_mul_f32_e32 v178, v172, v178
	v_mul_f32_e32 v179, v151, v213
	v_fmac_f32_e32 v179, v159, v221
	v_fmac_f32_e32 v179, v167, v229
	v_mul_f32_e32 v179, v173, v179
	v_lshlrev_b32_e32 v172, 16, v78
	v_and_b32_e32 v173, 0xffff0000, v78
	v_mul_f32_e32 v180, v152, v214
	v_fmac_f32_e32 v180, v160, v222
	v_fmac_f32_e32 v180, v168, v230
	v_mul_f32_e32 v180, v172, v180
	v_mul_f32_e32 v181, v153, v215
	v_fmac_f32_e32 v181, v161, v223
	v_fmac_f32_e32 v181, v169, v231
	v_mul_f32_e32 v181, v173, v181
	v_lshlrev_b32_e32 v172, 16, v79
	v_and_b32_e32 v173, 0xffff0000, v79
	v_mul_f32_e32 v182, v154, v216
	v_fmac_f32_e32 v182, v162, v224
	v_fmac_f32_e32 v182, v170, v232
	v_mul_f32_e32 v182, v172, v182
	v_mul_f32_e32 v183, v155, v217
	v_fmac_f32_e32 v183, v163, v225
	v_fmac_f32_e32 v183, v171, v233
	v_mul_f32_e32 v183, v173, v183
	v_cvt_pk_bf16_f32 v184, v176, v177
	v_cvt_pk_bf16_f32 v185, v178, v179
	v_cvt_pk_bf16_f32 v186, v180, v181
	v_cvt_pk_bf16_f32 v187, v182, v183
	v_add_u32_e32 v13, 0x1000, v16
	global_store_dwordx4 v13, v[184:187], s[14:15] nt
	s_nop 1
	v_lshlrev_b32_e32 v172, 16, v80
	v_and_b32_e32 v173, 0xffff0000, v80
	v_mul_f32_e32 v176, v148, v218
	v_fmac_f32_e32 v176, v156, v226
	v_fmac_f32_e32 v176, v164, v234
	v_mul_f32_e32 v176, v172, v176
	v_mul_f32_e32 v177, v149, v219
	v_fmac_f32_e32 v177, v157, v227
	v_fmac_f32_e32 v177, v165, v235
	v_mul_f32_e32 v177, v173, v177
	v_lshlrev_b32_e32 v172, 16, v81
	v_and_b32_e32 v173, 0xffff0000, v81
	v_mul_f32_e32 v178, v150, v220
	v_fmac_f32_e32 v178, v158, v228
	v_fmac_f32_e32 v178, v166, v236
	v_mul_f32_e32 v178, v172, v178
	v_mul_f32_e32 v179, v151, v221
	v_fmac_f32_e32 v179, v159, v229
	v_fmac_f32_e32 v179, v167, v237
	v_mul_f32_e32 v179, v173, v179
	v_lshlrev_b32_e32 v172, 16, v82
	v_and_b32_e32 v173, 0xffff0000, v82
	v_mul_f32_e32 v180, v152, v222
	v_fmac_f32_e32 v180, v160, v230
	v_fmac_f32_e32 v180, v168, v238
	v_mul_f32_e32 v180, v172, v180
	v_mul_f32_e32 v181, v153, v223
	v_fmac_f32_e32 v181, v161, v231
	v_fmac_f32_e32 v181, v169, v239
	v_mul_f32_e32 v181, v173, v181
	v_lshlrev_b32_e32 v172, 16, v83
	v_and_b32_e32 v173, 0xffff0000, v83
	v_mul_f32_e32 v182, v154, v224
	v_fmac_f32_e32 v182, v162, v232
	v_fmac_f32_e32 v182, v170, v240
	v_mul_f32_e32 v182, v172, v182
	v_mul_f32_e32 v183, v155, v225
	v_fmac_f32_e32 v183, v163, v233
	v_fmac_f32_e32 v183, v171, v241
	v_mul_f32_e32 v183, v173, v183
	v_cvt_pk_bf16_f32 v184, v176, v177
	v_cvt_pk_bf16_f32 v185, v178, v179
	v_cvt_pk_bf16_f32 v186, v180, v181
	v_cvt_pk_bf16_f32 v187, v182, v183
	v_add_u32_e32 v13, 0x1800, v16
	global_store_dwordx4 v13, v[184:187], s[14:15] nt
	s_nop 1
	s_waitcnt vmcnt(4)
	v_cmp_le_u32_e32 vcc, 2, v18
	s_nop 1
	v_cndmask_b32_e32 v84, 0, v84, vcc
	v_cndmask_b32_e32 v85, 0, v85, vcc
	v_cndmask_b32_e32 v86, 0, v86, vcc
	v_cndmask_b32_e32 v87, 0, v87, vcc
	v_cmp_le_u32_e32 vcc, 1, v18
	s_nop 1
	v_cndmask_b32_e32 v88, 0, v88, vcc
	v_cndmask_b32_e32 v89, 0, v89, vcc
	v_cndmask_b32_e32 v90, 0, v90, vcc
	v_cndmask_b32_e32 v91, 0, v91, vcc
	v_lshlrev_b32_e32 v172, 16, v84
	v_and_b32_e32 v173, 0xffff0000, v84
	v_lshlrev_b32_e32 v174, 16, v108
	v_and_b32_e32 v175, 0xffff0000, v108
	v_mul_f32_e32 v194, v172, v174
	v_mul_f32_e32 v195, v173, v175
	v_lshlrev_b32_e32 v172, 16, v85
	v_and_b32_e32 v173, 0xffff0000, v85
	v_lshlrev_b32_e32 v174, 16, v109
	v_and_b32_e32 v175, 0xffff0000, v109
	v_mul_f32_e32 v196, v172, v174
	v_mul_f32_e32 v197, v173, v175
	v_lshlrev_b32_e32 v172, 16, v86
	v_and_b32_e32 v173, 0xffff0000, v86
	v_lshlrev_b32_e32 v174, 16, v110
	v_and_b32_e32 v175, 0xffff0000, v110
	v_mul_f32_e32 v198, v172, v174
	v_mul_f32_e32 v199, v173, v175
	v_lshlrev_b32_e32 v172, 16, v87
	v_and_b32_e32 v173, 0xffff0000, v87
	v_lshlrev_b32_e32 v174, 16, v111
	v_and_b32_e32 v175, 0xffff0000, v111
	v_mul_f32_e32 v200, v172, v174
	v_mul_f32_e32 v201, v173, v175
	v_lshlrev_b32_e32 v172, 16, v88
	v_and_b32_e32 v173, 0xffff0000, v88
	v_lshlrev_b32_e32 v174, 16, v112
	v_and_b32_e32 v175, 0xffff0000, v112
	v_mul_f32_e32 v202, v172, v174
	v_mul_f32_e32 v203, v173, v175
	v_lshlrev_b32_e32 v172, 16, v89
	v_and_b32_e32 v173, 0xffff0000, v89
	v_lshlrev_b32_e32 v174, 16, v113
	v_and_b32_e32 v175, 0xffff0000, v113
	v_mul_f32_e32 v204, v172, v174
	v_mul_f32_e32 v205, v173, v175
	v_lshlrev_b32_e32 v172, 16, v90
	v_and_b32_e32 v173, 0xffff0000, v90
	v_lshlrev_b32_e32 v174, 16, v114
	v_and_b32_e32 v175, 0xffff0000, v114
	v_mul_f32_e32 v206, v172, v174
	v_mul_f32_e32 v207, v173, v175
	v_lshlrev_b32_e32 v172, 16, v91
	v_and_b32_e32 v173, 0xffff0000, v91
	v_lshlrev_b32_e32 v174, 16, v115
; __device__ __forceinline__ unsigned pk2(float lo, float hi) { return pg8::cvt_pk_bf16(lo, hi); }
; __device__ __forceinline__ void unpack8(const v4u w, float (&f)[8]) { f[0] = bflo(w.x); f[1] = bfhi(w.x); f[2] = bflo(w.y); f[3] = bfhi(w.y); f[4] = bflo(w.z); f[5] = bfhi(w.z); f[6] = bflo(w.w); f[7] = bfhi(w.w); }
; __device__ __forceinline__ void poolconv_phase(Frame& F, const float* conv_w_l) {
;     ...
;     for (int idx = gt; idx < M * 128; idx += NGT) {
;         const int row = idx >> 7, c8 = (idx & 127) * 8, t = row & (SEQ - 1);
;         float acc[8], a[8], b[8];
; #pragma unroll
;         for (int i = 0; i < 8; ++i) acc[i] = 0.f;
;         v4u la[3], lb[3];
; #pragma unroll
;         for (int j = 0; j < 3; ++j) { const int back = (t - 2 + j) >= 0 ? (2 - j) : 0; const bf16* pr = F.PROJ + (size_t)(row - back) * INWP; la[j] = *(const v4u*)(pr + O_CG + c8); lb[j] = *(const v4u*)(pr + O_UCONV + c8); }
;         const v4u lg = *(const v4u*)(F.PROJ + (size_t)row * INWP + O_BG + c8);
; #pragma unroll
;         for (int j = 0; j < 3; ++j) { const float wgt = (t - 2 + j) >= 0 ? 1.f : 0.f; unpack8(la[j], a); unpack8(lb[j], b);
;             const f32x4 w0 = *(const f32x4*)(conv_w_l + j * 1024 + c8) * wgt, w1 = *(const f32x4*)(conv_w_l + j * 1024 + c8 + 4) * wgt;
;             acc[0] += w0.x * (a[0] * b[0]); acc[1] += w0.y * (a[1] * b[1]); acc[2] += w0.z * (a[2] * b[2]); acc[3] += w0.w * (a[3] * b[3]);
;             acc[4] += w1.x * (a[4] * b[4]); acc[5] += w1.y * (a[5] * b[5]); acc[6] += w1.z * (a[6] * b[6]); acc[7] += w1.w * (a[7] * b[7]); }
;         unpack8(lg, a);
;         v4u o; o.x = pk2(a[0] * acc[0], a[1] * acc[1]); o.y = pk2(a[2] * acc[2], a[3] * acc[3]); o.z = pk2(a[4] * acc[4], a[5] * acc[5]); o.w = pk2(a[6] * acc[6], a[7] * acc[7]);
;         *(v4u*)(F.Y + (size_t)M * 1024 + (size_t)row * 1024 + c8) = o;
	v_and_b32_e32 v175, 0xffff0000, v115
	v_mul_f32_e32 v208, v172, v174
	v_mul_f32_e32 v209, v173, v175
	v_lshlrev_b32_e32 v172, 16, v92
	v_and_b32_e32 v173, 0xffff0000, v92
	v_lshlrev_b32_e32 v174, 16, v116
	v_and_b32_e32 v175, 0xffff0000, v116
	v_mul_f32_e32 v210, v172, v174
	v_mul_f32_e32 v211, v173, v175
	v_lshlrev_b32_e32 v172, 16, v93
	v_and_b32_e32 v173, 0xffff0000, v93
	v_lshlrev_b32_e32 v174, 16, v117
	v_and_b32_e32 v175, 0xffff0000, v117
	v_mul_f32_e32 v212, v172, v174
	v_mul_f32_e32 v213, v173, v175
	v_lshlrev_b32_e32 v172, 16, v94
	v_and_b32_e32 v173, 0xffff0000, v94
	v_lshlrev_b32_e32 v174, 16, v118
	v_and_b32_e32 v175, 0xffff0000, v118
	v_mul_f32_e32 v214, v172, v174
	v_mul_f32_e32 v215, v173, v175
	v_lshlrev_b32_e32 v172, 16, v95
	v_and_b32_e32 v173, 0xffff0000, v95
	v_lshlrev_b32_e32 v174, 16, v119
	v_and_b32_e32 v175, 0xffff0000, v119
	v_mul_f32_e32 v216, v172, v174
	v_mul_f32_e32 v217, v173, v175
	v_lshlrev_b32_e32 v172, 16, v96
	v_and_b32_e32 v173, 0xffff0000, v96
	v_lshlrev_b32_e32 v174, 16, v120
	v_and_b32_e32 v175, 0xffff0000, v120
	v_mul_f32_e32 v218, v172, v174
	v_mul_f32_e32 v219, v173, v175
	v_lshlrev_b32_e32 v172, 16, v97
	v_and_b32_e32 v173, 0xffff0000, v97
	v_lshlrev_b32_e32 v174, 16, v121
	v_and_b32_e32 v175, 0xffff0000, v121
	v_mul_f32_e32 v220, v172, v174
	v_mul_f32_e32 v221, v173, v175
	v_lshlrev_b32_e32 v172, 16, v98
	v_and_b32_e32 v173, 0xffff0000, v98
	v_lshlrev_b32_e32 v174, 16, v122
	v_and_b32_e32 v175, 0xffff0000, v122
	v_mul_f32_e32 v222, v172, v174
	v_mul_f32_e32 v223, v173, v175
	v_lshlrev_b32_e32 v172, 16, v99
	v_and_b32_e32 v173, 0xffff0000, v99
	v_lshlrev_b32_e32 v174, 16, v123
	v_and_b32_e32 v175, 0xffff0000, v123
	v_mul_f32_e32 v224, v172, v174
	v_mul_f32_e32 v225, v173, v175
	v_lshlrev_b32_e32 v172, 16, v100
	v_and_b32_e32 v173, 0xffff0000, v100
	v_lshlrev_b32_e32 v174, 16, v124
	v_and_b32_e32 v175, 0xffff0000, v124
	v_mul_f32_e32 v226, v172, v174
	v_mul_f32_e32 v227, v173, v175
	v_lshlrev_b32_e32 v172, 16, v101
	v_and_b32_e32 v173, 0xffff0000, v101
	v_lshlrev_b32_e32 v174, 16, v125
	v_and_b32_e32 v175, 0xffff0000, v125
	v_mul_f32_e32 v228, v172, v174
	v_mul_f32_e32 v229, v173, v175
	v_lshlrev_b32_e32 v172, 16, v102
	v_and_b32_e32 v173, 0xffff0000, v102
	v_lshlrev_b32_e32 v174, 16, v126
	v_and_b32_e32 v175, 0xffff0000, v126
	v_mul_f32_e32 v230, v172, v174
	v_mul_f32_e32 v231, v173, v175
	v_lshlrev_b32_e32 v172, 16, v103
	v_and_b32_e32 v173, 0xffff0000, v103
	v_lshlrev_b32_e32 v174, 16, v127
	v_and_b32_e32 v175, 0xffff0000, v127
	v_mul_f32_e32 v232, v172, v174
	v_mul_f32_e32 v233, v173, v175
	v_lshlrev_b32_e32 v172, 16, v104
	v_and_b32_e32 v173, 0xffff0000, v104
	v_lshlrev_b32_e32 v174, 16, v128
	v_and_b32_e32 v175, 0xffff0000, v128
	v_mul_f32_e32 v234, v172, v174
	v_mul_f32_e32 v235, v173, v175
	v_lshlrev_b32_e32 v172, 16, v105
	v_and_b32_e32 v173, 0xffff0000, v105
	v_lshlrev_b32_e32 v174, 16, v129
	v_and_b32_e32 v175, 0xffff0000, v129
	v_mul_f32_e32 v236, v172, v174
	v_mul_f32_e32 v237, v173, v175
	v_lshlrev_b32_e32 v172, 16, v106
	v_and_b32_e32 v173, 0xffff0000, v106
	v_lshlrev_b32_e32 v174, 16, v130
	v_and_b32_e32 v175, 0xffff0000, v130
	v_mul_f32_e32 v238, v172, v174
	v_mul_f32_e32 v239, v173, v175
	v_lshlrev_b32_e32 v172, 16, v107
	v_and_b32_e32 v173, 0xffff0000, v107
	v_lshlrev_b32_e32 v174, 16, v131
	v_and_b32_e32 v175, 0xffff0000, v131
	v_mul_f32_e32 v240, v172, v174
	v_mul_f32_e32 v241, v173, v175
	v_lshlrev_b32_e32 v172, 16, v132
	v_and_b32_e32 v173, 0xffff0000, v132
	v_mul_f32_e32 v176, v148, v194
	v_fmac_f32_e32 v176, v156, v202
	v_fmac_f32_e32 v176, v164, v210
	v_mul_f32_e32 v176, v172, v176
	v_mul_f32_e32 v177, v149, v195
	v_fmac_f32_e32 v177, v157, v203
	v_fmac_f32_e32 v177, v165, v211
	v_mul_f32_e32 v177, v173, v177
	v_lshlrev_b32_e32 v172, 16, v133
	v_and_b32_e32 v173, 0xffff0000, v133
	v_mul_f32_e32 v178, v150, v196
	v_fmac_f32_e32 v178, v158, v204
	v_fmac_f32_e32 v178, v166, v212
	v_mul_f32_e32 v178, v172, v178
	v_mul_f32_e32 v179, v151, v197
	v_fmac_f32_e32 v179, v159, v205
	v_fmac_f32_e32 v179, v167, v213
	v_mul_f32_e32 v179, v173, v179
	v_lshlrev_b32_e32 v172, 16, v134
	v_and_b32_e32 v173, 0xffff0000, v134
	v_mul_f32_e32 v180, v152, v198
	v_fmac_f32_e32 v180, v160, v206
	v_fmac_f32_e32 v180, v168, v214
	v_mul_f32_e32 v180, v172, v180
	v_mul_f32_e32 v181, v153, v199
	v_fmac_f32_e32 v181, v161, v207
	v_fmac_f32_e32 v181, v169, v215
	v_mul_f32_e32 v181, v173, v181
	v_lshlrev_b32_e32 v172, 16, v135
	v_and_b32_e32 v173, 0xffff0000, v135
	v_mul_f32_e32 v182, v154, v200
	v_fmac_f32_e32 v182, v162, v208
	v_fmac_f32_e32 v182, v170, v216
	v_mul_f32_e32 v182, v172, v182
	v_mul_f32_e32 v183, v155, v201
	v_fmac_f32_e32 v183, v163, v209
	v_fmac_f32_e32 v183, v171, v217
	v_mul_f32_e32 v183, v173, v183
	v_cvt_pk_bf16_f32 v184, v176, v177
	v_cvt_pk_bf16_f32 v185, v178, v179
	v_cvt_pk_bf16_f32 v186, v180, v181
; __device__ __forceinline__ unsigned pk2(float lo, float hi) { return pg8::cvt_pk_bf16(lo, hi); }
; __device__ __forceinline__ void unpack8(const v4u w, float (&f)[8]) { f[0] = bflo(w.x); f[1] = bfhi(w.x); f[2] = bflo(w.y); f[3] = bfhi(w.y); f[4] = bflo(w.z); f[5] = bfhi(w.z); f[6] = bflo(w.w); f[7] = bfhi(w.w); }
; __device__ __forceinline__ void poolconv_phase(Frame& F, const float* conv_w_l) {
;     ...
;     for (int idx = gt; idx < M * 128; idx += NGT) {
;         const int row = idx >> 7, c8 = (idx & 127) * 8, t = row & (SEQ - 1);
;         float acc[8], a[8], b[8];
; #pragma unroll
;         for (int i = 0; i < 8; ++i) acc[i] = 0.f;
;         v4u la[3], lb[3];
; #pragma unroll
;         for (int j = 0; j < 3; ++j) { const int back = (t - 2 + j) >= 0 ? (2 - j) : 0; const bf16* pr = F.PROJ + (size_t)(row - back) * INWP; la[j] = *(const v4u*)(pr + O_CG + c8); lb[j] = *(const v4u*)(pr + O_UCONV + c8); }
;         const v4u lg = *(const v4u*)(F.PROJ + (size_t)row * INWP + O_BG + c8);
; #pragma unroll
;         for (int j = 0; j < 3; ++j) { const float wgt = (t - 2 + j) >= 0 ? 1.f : 0.f; unpack8(la[j], a); unpack8(lb[j], b);
;             const f32x4 w0 = *(const f32x4*)(conv_w_l + j * 1024 + c8) * wgt, w1 = *(const f32x4*)(conv_w_l + j * 1024 + c8 + 4) * wgt;
;             acc[0] += w0.x * (a[0] * b[0]); acc[1] += w0.y * (a[1] * b[1]); acc[2] += w0.z * (a[2] * b[2]); acc[3] += w0.w * (a[3] * b[3]);
;             acc[4] += w1.x * (a[4] * b[4]); acc[5] += w1.y * (a[5] * b[5]); acc[6] += w1.z * (a[6] * b[6]); acc[7] += w1.w * (a[7] * b[7]); }
;         unpack8(lg, a);
;         v4u o; o.x = pk2(a[0] * acc[0], a[1] * acc[1]); o.y = pk2(a[2] * acc[2], a[3] * acc[3]); o.z = pk2(a[4] * acc[4], a[5] * acc[5]); o.w = pk2(a[6] * acc[6], a[7] * acc[7]);
;         *(v4u*)(F.Y + (size_t)M * 1024 + (size_t)row * 1024 + c8) = o;
	v_cvt_pk_bf16_f32 v187, v182, v183
	global_store_dwordx4 v17, v[184:187], s[14:15] nt
	s_nop 1
	v_lshlrev_b32_e32 v172, 16, v136
	v_and_b32_e32 v173, 0xffff0000, v136
	v_mul_f32_e32 v176, v148, v202
	v_fmac_f32_e32 v176, v156, v210
	v_fmac_f32_e32 v176, v164, v218
	v_mul_f32_e32 v176, v172, v176
	v_mul_f32_e32 v177, v149, v203
	v_fmac_f32_e32 v177, v157, v211
	v_fmac_f32_e32 v177, v165, v219
	v_mul_f32_e32 v177, v173, v177
	v_lshlrev_b32_e32 v172, 16, v137
	v_and_b32_e32 v173, 0xffff0000, v137
	v_mul_f32_e32 v178, v150, v204
	v_fmac_f32_e32 v178, v158, v212
	v_fmac_f32_e32 v178, v166, v220
	v_mul_f32_e32 v178, v172, v178
	v_mul_f32_e32 v179, v151, v205
	v_fmac_f32_e32 v179, v159, v213
	v_fmac_f32_e32 v179, v167, v221
	v_mul_f32_e32 v179, v173, v179
	v_lshlrev_b32_e32 v172, 16, v138
	v_and_b32_e32 v173, 0xffff0000, v138
	v_mul_f32_e32 v180, v152, v206
	v_fmac_f32_e32 v180, v160, v214
	v_fmac_f32_e32 v180, v168, v222
	v_mul_f32_e32 v180, v172, v180
	v_mul_f32_e32 v181, v153, v207
	v_fmac_f32_e32 v181, v161, v215
	v_fmac_f32_e32 v181, v169, v223
	v_mul_f32_e32 v181, v173, v181
	v_lshlrev_b32_e32 v172, 16, v139
	v_and_b32_e32 v173, 0xffff0000, v139
	v_mul_f32_e32 v182, v154, v208
	v_fmac_f32_e32 v182, v162, v216
	v_fmac_f32_e32 v182, v170, v224
	v_mul_f32_e32 v182, v172, v182
	v_mul_f32_e32 v183, v155, v209
	v_fmac_f32_e32 v183, v163, v217
	v_fmac_f32_e32 v183, v171, v225
	v_mul_f32_e32 v183, v173, v183
	v_cvt_pk_bf16_f32 v184, v176, v177
	v_cvt_pk_bf16_f32 v185, v178, v179
	v_cvt_pk_bf16_f32 v186, v180, v181
	v_cvt_pk_bf16_f32 v187, v182, v183
	v_add_u32_e32 v13, 0x800, v17
	global_store_dwordx4 v13, v[184:187], s[14:15] nt
	s_nop 1
	v_lshlrev_b32_e32 v172, 16, v140
	v_and_b32_e32 v173, 0xffff0000, v140
	v_mul_f32_e32 v176, v148, v210
	v_fmac_f32_e32 v176, v156, v218
	v_fmac_f32_e32 v176, v164, v226
	v_mul_f32_e32 v176, v172, v176
	v_mul_f32_e32 v177, v149, v211
	v_fmac_f32_e32 v177, v157, v219
	v_fmac_f32_e32 v177, v165, v227
	v_mul_f32_e32 v177, v173, v177
	v_lshlrev_b32_e32 v172, 16, v141
	v_and_b32_e32 v173, 0xffff0000, v141
	v_mul_f32_e32 v178, v150, v212
	v_fmac_f32_e32 v178, v158, v220
	v_fmac_f32_e32 v178, v166, v228
	v_mul_f32_e32 v178, v172, v178
	v_mul_f32_e32 v179, v151, v213
	v_fmac_f32_e32 v179, v159, v221
	v_fmac_f32_e32 v179, v167, v229
	v_mul_f32_e32 v179, v173, v179
	v_lshlrev_b32_e32 v172, 16, v142
	v_and_b32_e32 v173, 0xffff0000, v142
	v_mul_f32_e32 v180, v152, v214
	v_fmac_f32_e32 v180, v160, v222
	v_fmac_f32_e32 v180, v168, v230
	v_mul_f32_e32 v180, v172, v180
	v_mul_f32_e32 v181, v153, v215
	v_fmac_f32_e32 v181, v161, v223
	v_fmac_f32_e32 v181, v169, v231
	v_mul_f32_e32 v181, v173, v181
	v_lshlrev_b32_e32 v172, 16, v143
	v_and_b32_e32 v173, 0xffff0000, v143
	v_mul_f32_e32 v182, v154, v216
	v_fmac_f32_e32 v182, v162, v224
	v_fmac_f32_e32 v182, v170, v232
	v_mul_f32_e32 v182, v172, v182
	v_mul_f32_e32 v183, v155, v217
	v_fmac_f32_e32 v183, v163, v225
	v_fmac_f32_e32 v183, v171, v233
	v_mul_f32_e32 v183, v173, v183
	v_cvt_pk_bf16_f32 v184, v176, v177
	v_cvt_pk_bf16_f32 v185, v178, v179
	v_cvt_pk_bf16_f32 v186, v180, v181
	v_cvt_pk_bf16_f32 v187, v182, v183
	v_add_u32_e32 v13, 0x1000, v17
	global_store_dwordx4 v13, v[184:187], s[14:15] nt
	s_nop 1
	v_lshlrev_b32_e32 v172, 16, v144
	v_and_b32_e32 v173, 0xffff0000, v144
	v_mul_f32_e32 v176, v148, v218
	v_fmac_f32_e32 v176, v156, v226
	v_fmac_f32_e32 v176, v164, v234
	v_mul_f32_e32 v176, v172, v176
	v_mul_f32_e32 v177, v149, v219
	v_fmac_f32_e32 v177, v157, v227
	v_fmac_f32_e32 v177, v165, v235
	v_mul_f32_e32 v177, v173, v177
	v_lshlrev_b32_e32 v172, 16, v145
	v_and_b32_e32 v173, 0xffff0000, v145
	v_mul_f32_e32 v178, v150, v220
	v_fmac_f32_e32 v178, v158, v228
	v_fmac_f32_e32 v178, v166, v236
	v_mul_f32_e32 v178, v172, v178
	v_mul_f32_e32 v179, v151, v221
	v_fmac_f32_e32 v179, v159, v229
	v_fmac_f32_e32 v179, v167, v237
	v_mul_f32_e32 v179, v173, v179
	v_lshlrev_b32_e32 v172, 16, v146
	v_and_b32_e32 v173, 0xffff0000, v146
	v_mul_f32_e32 v180, v152, v222
	v_fmac_f32_e32 v180, v160, v230
	v_fmac_f32_e32 v180, v168, v238
	v_mul_f32_e32 v180, v172, v180
	v_mul_f32_e32 v181, v153, v223
	v_fmac_f32_e32 v181, v161, v231
	v_fmac_f32_e32 v181, v169, v239
	v_mul_f32_e32 v181, v173, v181
	v_lshlrev_b32_e32 v172, 16, v147
	v_and_b32_e32 v173, 0xffff0000, v147
	v_mul_f32_e32 v182, v154, v224
	v_fmac_f32_e32 v182, v162, v232
	v_fmac_f32_e32 v182, v170, v240
	v_mul_f32_e32 v182, v172, v182
	v_mul_f32_e32 v183, v155, v225
	v_fmac_f32_e32 v183, v163, v233
	v_fmac_f32_e32 v183, v171, v241
	v_mul_f32_e32 v183, v173, v183
	v_cvt_pk_bf16_f32 v184, v176, v177
	v_cvt_pk_bf16_f32 v185, v178, v179
	v_cvt_pk_bf16_f32 v186, v180, v181
	v_cvt_pk_bf16_f32 v187, v182, v183
	v_add_u32_e32 v13, 0x1800, v17
	global_store_dwordx4 v13, v[184:187], s[14:15] nt
	s_nop 1
	s_movk_i32 s8, 0x1000
	s_mov_b32 s20, 0xff800000
	s_mov_b64 s[2:3], exec
